# v16 + dead address-forming VALU removed from the 8 non-gather GEMM K-loops (left over from the LDS-DMA rewrite)
# speedup vs baseline: 1.0027x; 1.0008x over previous
.LBB0_249:
	s_add_u32 s31, s26, 0xfffc0080
	s_addc_u32 s33, s27, -1
	s_add_i32 s34, 0, 0x10000
	v_add_u32_e32 v0, s34, v138
	ds_read_b128 v[140:143], v0
	ds_read_b128 v[144:147], v0 offset:1024
	ds_read_b128 v[148:151], v0 offset:2048
	ds_read_b128 v[152:155], v0 offset:3072
	s_cmp_eq_u32 s30, 12
	s_cselect_b32 s49, s3, s33
	s_cselect_b32 s48, s5, s31
	s_cselect_b32 s47, s20, s25
	s_cselect_b32 s46, s21, s22
	ds_read_b128 v[156:159], v139
	ds_read_b128 v[160:163], v139 offset:1024
	ds_read_b128 v[172:175], v139 offset:2048
	ds_read_b128 v[176:179], v139 offset:3072
	ds_read_b128 v[180:183], v139 offset:4096
	ds_read_b128 v[184:187], v139 offset:5120
	ds_read_b128 v[188:191], v139 offset:6144
	ds_read_b128 v[192:195], v139 offset:7168
	s_nop 0
	s_nop 0
	s_waitcnt lgkmcnt(8)
	s_barrier
	s_waitcnt lgkmcnt(0)
	s_setprio 1
	v_mov_b64_e32 v[50:51], v[164:165]
	s_waitcnt lgkmcnt(0)
	v_mfma_scale_f32_16x16x128_f8f6f4 v[98:101], v[156:163], v[148:155], v[98:101], v202, v202 op_sel_hi:[0,0,0]
	v_mov_b64_e32 v[52:53], v[166:167]
	v_mfma_scale_f32_16x16x128_f8f6f4 v[164:167], v[172:179], v[140:147], v[118:121], v202, v202 op_sel_hi:[0,0,0]
	s_add_i32 m0, s1, 0xc000
	v_mfma_scale_f32_16x16x128_f8f6f4 v[90:93], v[180:187], v[148:155], v[90:93], v202, v202 op_sel_hi:[0,0,0]
	global_load_lds_dwordx4 v136, s[26:27]
	v_mfma_scale_f32_16x16x128_f8f6f4 v[130:133], v[156:163], v[140:147], v[126:129], v202, v202 op_sel_hi:[0,0,0]
	v_mfma_scale_f32_16x16x128_f8f6f4 v[168:171], v[172:179], v[148:155], v[86:89], v202, v202 op_sel_hi:[0,0,0]
	s_add_i32 m0, s1, 0xe000
	v_mfma_scale_f32_16x16x128_f8f6f4 v[196:199], v[180:187], v[140:147], v[122:125], v202, v202 op_sel_hi:[0,0,0]
	global_load_lds_dwordx4 v137, s[26:27]
	v_mfma_scale_f32_16x16x128_f8f6f4 v[206:209], v[188:195], v[140:147], v[114:117], v202, v202 op_sel_hi:[0,0,0]
	v_mfma_scale_f32_16x16x128_f8f6f4 v[210:213], v[188:195], v[148:155], v[82:85], v202, v202 op_sel_hi:[0,0,0]
	s_setprio 0
	s_barrier
	s_add_i32 s31, 0, 0x14000
	v_add_u32_e32 v0, s31, v138
	s_nop 2
	ds_read_b128 v[82:85], v0
	ds_read_b128 v[86:89], v0 offset:1024
	ds_read_b128 v[114:117], v0 offset:2048
	ds_read_b128 v[118:121], v0 offset:3072
	s_add_i32 s33, s34, s73
	s_nop 0
	s_nop 0
	s_barrier
	s_waitcnt lgkmcnt(0)
	s_setprio 1
	s_waitcnt lgkmcnt(0)
	v_mfma_scale_f32_16x16x128_f8f6f4 v[66:69], v[156:163], v[82:89], v[66:69], v202, v202 op_sel_hi:[0,0,0]
	v_mfma_scale_f32_16x16x128_f8f6f4 v[38:41], v[156:163], v[114:121], v[38:41], v202, v202 op_sel_hi:[0,0,0]
	s_mov_b32 m0, s33
	v_mfma_scale_f32_16x16x128_f8f6f4 v[58:61], v[180:187], v[82:89], v[58:61], v202, v202 op_sel_hi:[0,0,0]
	global_load_lds_dwordx4 v136, s[46:47]
	v_mfma_scale_f32_16x16x128_f8f6f4 v[214:217], v[172:179], v[82:89], v[54:57], v202, v202 op_sel_hi:[0,0,0]
	v_mfma_scale_f32_16x16x128_f8f6f4 v[172:175], v[172:179], v[114:121], v[22:25], v202, v202 op_sel_hi:[0,0,0]
	s_add_i32 m0, s33, 0x2000
	v_mfma_scale_f32_16x16x128_f8f6f4 v[176:179], v[180:187], v[114:121], v[30:33], v202, v202 op_sel_hi:[0,0,0]
	global_load_lds_dwordx4 v137, s[46:47]
	v_mfma_scale_f32_16x16x128_f8f6f4 v[180:183], v[188:195], v[82:89], v[18:21], v202, v202 op_sel_hi:[0,0,0]
	v_mfma_scale_f32_16x16x128_f8f6f4 v[184:187], v[188:195], v[114:121], v[50:53], v202, v202 op_sel_hi:[0,0,0]
	s_setprio 0
	s_barrier
	s_nop 1
	ds_read_b128 v[18:21], v139 offset:16384
	ds_read_b128 v[22:25], v139 offset:17408
	ds_read_b128 v[50:53], v139 offset:18432
	ds_read_b128 v[54:57], v139 offset:19456
	ds_read_b128 v[122:125], v139 offset:20480
	ds_read_b128 v[126:129], v139 offset:21504
	ds_read_b128 v[156:159], v139 offset:22528
	ds_read_b128 v[160:163], v139 offset:23552
	s_nop 0
	s_nop 0
	s_barrier
	s_waitcnt lgkmcnt(0)
	s_setprio 1
	s_waitcnt lgkmcnt(0)
	v_mfma_scale_f32_16x16x128_f8f6f4 v[110:113], v[18:25], v[140:147], v[110:113], v202, v202 op_sel_hi:[0,0,0]
	v_mfma_scale_f32_16x16x128_f8f6f4 v[78:81], v[18:25], v[148:155], v[78:81], v202, v202 op_sel_hi:[0,0,0]
	s_mov_b32 m0, s1
	v_mfma_scale_f32_16x16x128_f8f6f4 v[102:105], v[50:57], v[140:147], v[102:105], v202, v202 op_sel_hi:[0,0,0]
	global_load_lds_dwordx4 v136, s[48:49]
	v_mfma_scale_f32_16x16x128_f8f6f4 v[106:109], v[122:129], v[140:147], v[106:109], v202, v202 op_sel_hi:[0,0,0]
	v_mfma_scale_f32_16x16x128_f8f6f4 v[94:97], v[156:163], v[140:147], v[94:97], v202, v202 op_sel_hi:[0,0,0]
	s_mov_b32 m0, s13
	v_mfma_scale_f32_16x16x128_f8f6f4 v[62:65], v[156:163], v[148:155], v[62:65], v202, v202 op_sel_hi:[0,0,0]
	global_load_lds_dwordx4 v137, s[48:49]
	v_mfma_scale_f32_16x16x128_f8f6f4 v[218:221], v[50:57], v[148:155], v[70:73], v202, v202 op_sel_hi:[0,0,0]
	v_mfma_scale_f32_16x16x128_f8f6f4 v[222:225], v[122:129], v[148:155], v[74:77], v202, v202 op_sel_hi:[0,0,0]
	s_setprio 0
	s_barrier
	s_add_u32 s34, s46, 0x40000
	s_addc_u32 s35, s47, 0
	s_add_i32 s31, s31, s73
	s_mov_b32 s100, s31
	s_nop 0
	s_add_i32 s101, s31, 0x2000
	s_nop 0
	s_waitcnt vmcnt(4)
	s_barrier
	s_setprio 1
	v_mfma_scale_f32_16x16x128_f8f6f4 v[34:37], v[50:57], v[82:89], v[34:37], v202, v202 op_sel_hi:[0,0,0]
	v_mfma_scale_f32_16x16x128_f8f6f4 v[226:229], v[18:25], v[82:89], v[46:49], v202, v202 op_sel_hi:[0,0,0]
	s_mov_b32 m0, s100
	v_mfma_scale_f32_16x16x128_f8f6f4 v[230:233], v[18:25], v[114:121], v[14:17], v202, v202 op_sel_hi:[0,0,0]
	global_load_lds_dwordx4 v136, s[34:35]
	v_mfma_scale_f32_16x16x128_f8f6f4 v[234:237], v[50:57], v[114:121], v[6:9], v202, v202 op_sel_hi:[0,0,0]
	v_mfma_scale_f32_16x16x128_f8f6f4 v[238:241], v[122:129], v[82:89], v[42:45], v202, v202 op_sel_hi:[0,0,0]
	s_mov_b32 m0, s101
	v_mfma_scale_f32_16x16x128_f8f6f4 v[242:245], v[122:129], v[114:121], v[10:13], v202, v202 op_sel_hi:[0,0,0]
	global_load_lds_dwordx4 v137, s[34:35]
	v_mfma_scale_f32_16x16x128_f8f6f4 v[246:249], v[156:163], v[82:89], v[26:29], v202, v202 op_sel_hi:[0,0,0]
	v_mfma_scale_f32_16x16x128_f8f6f4 v[50:53], v[156:163], v[114:121], v[2:5], v202, v202 op_sel_hi:[0,0,0]
	s_setprio 0
	s_add_i32 s31, 0, 0x18000
	v_add_u32_e32 v0, s31, v138
	s_barrier
	s_nop 2
	ds_read_b128 v[2:5], v0
	ds_read_b128 v[6:9], v0 offset:1024
	ds_read_b128 v[10:13], v0 offset:2048
	ds_read_b128 v[14:17], v0 offset:3072
	s_add_u32 s34, s48, 0x40000
	ds_read_b128 v[18:21], v139 offset:32768
	ds_read_b128 v[22:25], v139 offset:33792
	ds_read_b128 v[26:29], v139 offset:34816
	ds_read_b128 v[30:33], v139 offset:35840
	ds_read_b128 v[42:45], v139 offset:36864
	ds_read_b128 v[46:49], v139 offset:37888
	ds_read_b128 v[70:73], v139 offset:38912
	ds_read_b128 v[74:77], v139 offset:39936
	s_addc_u32 s35, s49, 0
	s_nop 0
	s_nop 0
	s_waitcnt lgkmcnt(8)
	s_barrier
	s_waitcnt lgkmcnt(0)
	s_setprio 1
	s_waitcnt lgkmcnt(0)
	v_mfma_scale_f32_16x16x128_f8f6f4 v[126:129], v[18:25], v[2:9], v[130:133], v202, v202 op_sel_hi:[0,0,0]
	v_mfma_scale_f32_16x16x128_f8f6f4 v[98:101], v[18:25], v[10:17], v[98:101], v202, v202 op_sel_hi:[0,0,0]
	s_mov_b32 m0, s14
	v_mfma_scale_f32_16x16x128_f8f6f4 v[118:121], v[26:33], v[2:9], v[164:167], v202, v202 op_sel_hi:[0,0,0]
	global_load_lds_dwordx4 v136, s[34:35]
	v_mfma_scale_f32_16x16x128_f8f6f4 v[86:89], v[26:33], v[10:17], v[168:171], v202, v202 op_sel_hi:[0,0,0]
	v_mfma_scale_f32_16x16x128_f8f6f4 v[122:125], v[42:49], v[2:9], v[196:199], v202, v202 op_sel_hi:[0,0,0]
	s_mov_b32 m0, s15
	v_mfma_scale_f32_16x16x128_f8f6f4 v[90:93], v[42:49], v[10:17], v[90:93], v202, v202 op_sel_hi:[0,0,0]
	global_load_lds_dwordx4 v137, s[34:35]
	v_mfma_scale_f32_16x16x128_f8f6f4 v[114:117], v[70:77], v[2:9], v[206:209], v202, v202 op_sel_hi:[0,0,0]
	v_mfma_scale_f32_16x16x128_f8f6f4 v[82:85], v[70:77], v[10:17], v[210:213], v202, v202 op_sel_hi:[0,0,0]
	s_setprio 0
	s_barrier
	s_add_i32 s33, 0, 0x1c000
	v_add_u32_e32 v0, s33, v138
	ds_read_b128 v[140:143], v0
	ds_read_b128 v[144:147], v0 offset:1024
	ds_read_b128 v[148:151], v0 offset:2048
	ds_read_b128 v[152:155], v0 offset:3072
	s_add_i32 s31, s31, s73
	v_mov_b32_e32 v0, v137
	v_lshl_add_u64 v[54:55], s[46:47], 0, v[0:1]
	v_lshl_add_u64 v[54:55], v[54:55], 0, s[66:67]
	s_barrier
	s_waitcnt lgkmcnt(0)
	s_setprio 1
	s_waitcnt lgkmcnt(0)
	v_mfma_scale_f32_16x16x128_f8f6f4 v[66:69], v[18:25], v[140:147], v[66:69], v202, v202 op_sel_hi:[0,0,0]
	v_mfma_scale_f32_16x16x128_f8f6f4 v[38:41], v[18:25], v[148:155], v[38:41], v202, v202 op_sel_hi:[0,0,0]
	s_add_u32 s98, s46, s66
	s_addc_u32 s99, s47, s67
	s_mov_b32 m0, s31
	v_mfma_scale_f32_16x16x128_f8f6f4 v[54:57], v[26:33], v[140:147], v[214:217], v202, v202 op_sel_hi:[0,0,0]
	global_load_lds_dwordx4 v136, s[98:99]
	v_mfma_scale_f32_16x16x128_f8f6f4 v[22:25], v[26:33], v[148:155], v[172:175], v202, v202 op_sel_hi:[0,0,0]
	v_mfma_scale_f32_16x16x128_f8f6f4 v[58:61], v[42:49], v[140:147], v[58:61], v202, v202 op_sel_hi:[0,0,0]
	s_add_i32 m0, s31, 0x2000
	v_mfma_scale_f32_16x16x128_f8f6f4 v[30:33], v[42:49], v[148:155], v[176:179], v202, v202 op_sel_hi:[0,0,0]
	global_load_lds_dwordx4 v137, s[98:99]
	v_mfma_scale_f32_16x16x128_f8f6f4 v[18:21], v[70:77], v[140:147], v[180:183], v202, v202 op_sel_hi:[0,0,0]
	v_mfma_scale_f32_16x16x128_f8f6f4 v[164:167], v[70:77], v[148:155], v[184:187], v202, v202 op_sel_hi:[0,0,0]
	s_setprio 0
	s_barrier
	ds_read_b128 v[156:159], v139 offset:49152
	ds_read_b128 v[160:163], v139 offset:50176
	ds_read_b128 v[172:175], v139 offset:51200
	ds_read_b128 v[176:179], v139 offset:52224
	ds_read_b128 v[180:183], v139 offset:53248
	ds_read_b128 v[184:187], v139 offset:54272
	ds_read_b128 v[188:191], v139 offset:55296
	ds_read_b128 v[192:195], v139 offset:56320
	v_mov_b32_e32 v0, v137
	v_lshl_add_u64 v[26:27], s[48:49], 0, v[0:1]
	v_lshl_add_u64 v[26:27], v[26:27], 0, s[66:67]
	s_barrier
	s_waitcnt lgkmcnt(0)
	s_setprio 1
	s_waitcnt lgkmcnt(0)
	v_mfma_scale_f32_16x16x128_f8f6f4 v[110:113], v[156:163], v[2:9], v[110:113], v202, v202 op_sel_hi:[0,0,0]
	v_mfma_scale_f32_16x16x128_f8f6f4 v[78:81], v[156:163], v[10:17], v[78:81], v202, v202 op_sel_hi:[0,0,0]
	s_add_u32 s98, s48, s66
	s_addc_u32 s99, s49, s67
	s_mov_b32 m0, s17
	v_mfma_scale_f32_16x16x128_f8f6f4 v[102:105], v[172:179], v[2:9], v[102:105], v202, v202 op_sel_hi:[0,0,0]
	global_load_lds_dwordx4 v136, s[98:99]
	v_mfma_scale_f32_16x16x128_f8f6f4 v[70:73], v[172:179], v[10:17], v[218:221], v202, v202 op_sel_hi:[0,0,0]
	v_mfma_scale_f32_16x16x128_f8f6f4 v[106:109], v[180:187], v[2:9], v[106:109], v202, v202 op_sel_hi:[0,0,0]
	s_mov_b32 m0, s18
	v_mfma_scale_f32_16x16x128_f8f6f4 v[74:77], v[180:187], v[10:17], v[222:225], v202, v202 op_sel_hi:[0,0,0]
	global_load_lds_dwordx4 v137, s[98:99]
	v_mfma_scale_f32_16x16x128_f8f6f4 v[94:97], v[188:195], v[2:9], v[94:97], v202, v202 op_sel_hi:[0,0,0]
	v_mfma_scale_f32_16x16x128_f8f6f4 v[62:65], v[188:195], v[10:17], v[62:65], v202, v202 op_sel_hi:[0,0,0]
	s_setprio 0
	s_barrier
	s_add_u32 s34, s46, 0x40080
	s_addc_u32 s35, s47, 0
	s_add_i32 s31, s33, s73
	s_nop 0
	s_nop 0
	s_waitcnt vmcnt(4)
	s_barrier
	s_setprio 1
	v_mfma_scale_f32_16x16x128_f8f6f4 v[46:49], v[156:163], v[140:147], v[226:229], v202, v202 op_sel_hi:[0,0,0]
	v_mfma_scale_f32_16x16x128_f8f6f4 v[14:17], v[156:163], v[148:155], v[230:233], v202, v202 op_sel_hi:[0,0,0]
	s_mov_b32 m0, s31
	v_mfma_scale_f32_16x16x128_f8f6f4 v[34:37], v[172:179], v[140:147], v[34:37], v202, v202 op_sel_hi:[0,0,0]
	global_load_lds_dwordx4 v136, s[34:35]
	v_mfma_scale_f32_16x16x128_f8f6f4 v[6:9], v[172:179], v[148:155], v[234:237], v202, v202 op_sel_hi:[0,0,0]
	v_mfma_scale_f32_16x16x128_f8f6f4 v[42:45], v[180:187], v[140:147], v[238:241], v202, v202 op_sel_hi:[0,0,0]
	s_add_i32 m0, s31, 0x2000
	v_mfma_scale_f32_16x16x128_f8f6f4 v[10:13], v[180:187], v[148:155], v[242:245], v202, v202 op_sel_hi:[0,0,0]
	global_load_lds_dwordx4 v137, s[34:35]
	v_mfma_scale_f32_16x16x128_f8f6f4 v[26:29], v[188:195], v[140:147], v[246:249], v202, v202 op_sel_hi:[0,0,0]
	v_mfma_scale_f32_16x16x128_f8f6f4 v[2:5], v[188:195], v[148:155], v[50:53], v202, v202 op_sel_hi:[0,0,0]
	s_setprio 0
	s_add_i32 s30, s30, 2
	s_add_u32 s26, s26, 0x100
	s_addc_u32 s27, s27, 0
	s_add_u32 s22, s22, 0x100
	s_addc_u32 s25, s25, 0
	s_cmp_gt_u32 s30, 13
	s_barrier
	s_cbranch_scc0 .LBB0_249

.LBB0_278:
	s_add_u32 s6, s4, 0xfffc0080
	s_addc_u32 s7, s5, -1
	s_add_i32 s25, 0, 0x10000
	v_add_u32_e32 v0, s25, v207
	ds_read_b128 v[52:55], v0
	ds_read_b128 v[56:59], v0 offset:1024
	ds_read_b128 v[68:71], v0 offset:2048
	ds_read_b128 v[72:75], v0 offset:3072
	s_cmp_eq_u32 s17, 12
	s_cselect_b32 s11, s3, s7
	s_cselect_b32 s10, s9, s6
	s_cselect_b32 s7, s12, s16
	s_cselect_b32 s6, s13, s15
	ds_read_b128 v[84:87], v208
	ds_read_b128 v[88:91], v208 offset:1024
	ds_read_b128 v[92:95], v208 offset:2048
	ds_read_b128 v[96:99], v208 offset:3072
	ds_read_b128 v[172:175], v208 offset:4096
	ds_read_b128 v[176:179], v208 offset:5120
	ds_read_b128 v[180:183], v208 offset:6144
	ds_read_b128 v[184:187], v208 offset:7168
	s_nop 0
	s_nop 0
	s_waitcnt lgkmcnt(8)
	s_barrier
	s_waitcnt lgkmcnt(0)
	s_setprio 1
	s_waitcnt lgkmcnt(0)
	v_mfma_scale_f32_16x16x128_f8f6f4 v[164:167], v[52:59], v[84:91], v[164:167], v202, v202 op_sel_hi:[0,0,0]
	v_mfma_scale_f32_16x16x128_f8f6f4 v[160:163], v[68:75], v[84:91], v[160:163], v202, v202 op_sel_hi:[0,0,0]
	s_add_i32 m0, s18, 0xc000
	v_mfma_scale_f32_16x16x128_f8f6f4 v[156:159], v[52:59], v[92:99], v[156:159], v202, v202 op_sel_hi:[0,0,0]
	global_load_lds_dwordx4 v205, s[4:5]
	v_mfma_scale_f32_16x16x128_f8f6f4 v[152:155], v[68:75], v[92:99], v[152:155], v202, v202 op_sel_hi:[0,0,0]
	v_mfma_scale_f32_16x16x128_f8f6f4 v[148:151], v[52:59], v[172:179], v[148:151], v202, v202 op_sel_hi:[0,0,0]
	s_add_i32 m0, s18, 0xe000
	v_mfma_scale_f32_16x16x128_f8f6f4 v[188:191], v[68:75], v[172:179], v[144:147], v202, v202 op_sel_hi:[0,0,0]
	global_load_lds_dwordx4 v206, s[4:5]
	v_mfma_scale_f32_16x16x128_f8f6f4 v[192:195], v[52:59], v[180:187], v[136:139], v202, v202 op_sel_hi:[0,0,0]
	v_mfma_scale_f32_16x16x128_f8f6f4 v[196:199], v[68:75], v[180:187], v[132:135], v202, v202 op_sel_hi:[0,0,0]
	s_setprio 0
	s_barrier
	s_add_i32 s30, 0, 0x14000
	v_add_u32_e32 v0, s30, v207
	s_nop 2
	ds_read_b128 v[132:135], v0
	ds_read_b128 v[136:139], v0 offset:1024
	ds_read_b128 v[140:143], v0 offset:2048
	ds_read_b128 v[144:147], v0 offset:3072
	s_add_i32 s25, s25, s73
	s_nop 0
	s_nop 0
	s_barrier
	s_waitcnt lgkmcnt(0)
	s_setprio 1
	s_waitcnt lgkmcnt(0)
	v_mfma_scale_f32_16x16x128_f8f6f4 v[128:131], v[132:139], v[84:91], v[128:131], v202, v202 op_sel_hi:[0,0,0]
	v_mfma_scale_f32_16x16x128_f8f6f4 v[124:127], v[140:147], v[84:91], v[124:127], v202, v202 op_sel_hi:[0,0,0]
	s_mov_b32 m0, s25
	v_mfma_scale_f32_16x16x128_f8f6f4 v[120:123], v[132:139], v[92:99], v[120:123], v202, v202 op_sel_hi:[0,0,0]
	global_load_lds_dwordx4 v205, s[6:7]
	v_mfma_scale_f32_16x16x128_f8f6f4 v[116:119], v[140:147], v[92:99], v[116:119], v202, v202 op_sel_hi:[0,0,0]
	v_mfma_scale_f32_16x16x128_f8f6f4 v[210:213], v[132:139], v[172:179], v[112:115], v202, v202 op_sel_hi:[0,0,0]
	s_add_i32 m0, s25, 0x2000
	v_mfma_scale_f32_16x16x128_f8f6f4 v[172:175], v[140:147], v[172:179], v[108:111], v202, v202 op_sel_hi:[0,0,0]
	global_load_lds_dwordx4 v206, s[6:7]
	v_mfma_scale_f32_16x16x128_f8f6f4 v[176:179], v[132:139], v[180:187], v[104:107], v202, v202 op_sel_hi:[0,0,0]
	v_mfma_scale_f32_16x16x128_f8f6f4 v[180:183], v[140:147], v[180:187], v[100:103], v202, v202 op_sel_hi:[0,0,0]
	s_setprio 0
	s_barrier
	ds_read_b128 v[84:87], v208 offset:16384
	ds_read_b128 v[88:91], v208 offset:17408
	ds_read_b128 v[92:95], v208 offset:18432
	ds_read_b128 v[96:99], v208 offset:19456
	ds_read_b128 v[100:103], v208 offset:20480
	ds_read_b128 v[104:107], v208 offset:21504
	ds_read_b128 v[108:111], v208 offset:22528
	ds_read_b128 v[112:115], v208 offset:23552
	s_nop 0
	s_nop 0
	s_barrier
	s_waitcnt lgkmcnt(0)
	s_setprio 1
	s_waitcnt lgkmcnt(0)
	v_mfma_scale_f32_16x16x128_f8f6f4 v[80:83], v[52:59], v[84:91], v[80:83], v202, v202 op_sel_hi:[0,0,0]
	v_mfma_scale_f32_16x16x128_f8f6f4 v[76:79], v[68:75], v[84:91], v[76:79], v202, v202 op_sel_hi:[0,0,0]
	s_mov_b32 m0, s18
	v_mfma_scale_f32_16x16x128_f8f6f4 v[64:67], v[52:59], v[92:99], v[64:67], v202, v202 op_sel_hi:[0,0,0]
	global_load_lds_dwordx4 v205, s[10:11]
	v_mfma_scale_f32_16x16x128_f8f6f4 v[60:63], v[68:75], v[92:99], v[60:63], v202, v202 op_sel_hi:[0,0,0]
	v_mfma_scale_f32_16x16x128_f8f6f4 v[184:187], v[52:59], v[100:107], v[48:51], v202, v202 op_sel_hi:[0,0,0]
	s_mov_b32 m0, s19
	v_mfma_scale_f32_16x16x128_f8f6f4 v[214:217], v[68:75], v[100:107], v[44:47], v202, v202 op_sel_hi:[0,0,0]
	global_load_lds_dwordx4 v206, s[10:11]
	v_mfma_scale_f32_16x16x128_f8f6f4 v[218:221], v[52:59], v[108:115], v[40:43], v202, v202 op_sel_hi:[0,0,0]
	v_mfma_scale_f32_16x16x128_f8f6f4 v[222:225], v[68:75], v[108:115], v[36:39], v202, v202 op_sel_hi:[0,0,0]
	s_setprio 0
	s_barrier
	s_add_u32 s26, s6, 0x40000
	s_addc_u32 s27, s7, 0
	s_add_i32 s25, s30, s73
	s_mov_b32 s100, s25
	s_nop 0
	s_add_i32 s101, s25, 0x2000
	s_nop 0
	s_waitcnt vmcnt(4)
	s_barrier
	s_setprio 1
	v_mfma_scale_f32_16x16x128_f8f6f4 v[226:229], v[132:139], v[84:91], v[32:35], v202, v202 op_sel_hi:[0,0,0]
	v_mfma_scale_f32_16x16x128_f8f6f4 v[230:233], v[140:147], v[84:91], v[28:31], v202, v202 op_sel_hi:[0,0,0]
	s_mov_b32 m0, s100
	v_mfma_scale_f32_16x16x128_f8f6f4 v[234:237], v[132:139], v[92:99], v[24:27], v202, v202 op_sel_hi:[0,0,0]
	global_load_lds_dwordx4 v205, s[26:27]
	v_mfma_scale_f32_16x16x128_f8f6f4 v[238:241], v[140:147], v[92:99], v[20:23], v202, v202 op_sel_hi:[0,0,0]
	v_mfma_scale_f32_16x16x128_f8f6f4 v[242:245], v[132:139], v[100:107], v[16:19], v202, v202 op_sel_hi:[0,0,0]
	s_mov_b32 m0, s101
	v_mfma_scale_f32_16x16x128_f8f6f4 v[246:249], v[140:147], v[100:107], v[12:15], v202, v202 op_sel_hi:[0,0,0]
	global_load_lds_dwordx4 v206, s[26:27]
	v_mfma_scale_f32_16x16x128_f8f6f4 v[168:171], v[132:139], v[108:115], v[8:11], v202, v202 op_sel_hi:[0,0,0]
	v_mfma_scale_f32_16x16x128_f8f6f4 v[140:143], v[140:147], v[108:115], v[4:7], v202, v202 op_sel_hi:[0,0,0]
	s_setprio 0
	s_add_i32 s25, 0, 0x18000
	v_add_u32_e32 v0, s25, v207
	s_barrier
	s_nop 2
	ds_read_b128 v[2:5], v0
	ds_read_b128 v[6:9], v0 offset:1024
	ds_read_b128 v[10:13], v0 offset:2048
	ds_read_b128 v[14:17], v0 offset:3072
	s_add_u32 s26, s10, 0x40000
	ds_read_b128 v[18:21], v208 offset:32768
	ds_read_b128 v[22:25], v208 offset:33792
	ds_read_b128 v[26:29], v208 offset:34816
	ds_read_b128 v[30:33], v208 offset:35840
	ds_read_b128 v[34:37], v208 offset:36864
	ds_read_b128 v[38:41], v208 offset:37888
	ds_read_b128 v[42:45], v208 offset:38912
	ds_read_b128 v[46:49], v208 offset:39936
	s_addc_u32 s27, s11, 0
	s_nop 0
	s_nop 0
	s_waitcnt lgkmcnt(8)
	s_barrier
	s_waitcnt lgkmcnt(0)
	s_setprio 1
	s_waitcnt lgkmcnt(0)
	v_mfma_scale_f32_16x16x128_f8f6f4 v[164:167], v[2:9], v[18:25], v[164:167], v202, v202 op_sel_hi:[0,0,0]
	v_mfma_scale_f32_16x16x128_f8f6f4 v[160:163], v[10:17], v[18:25], v[160:163], v202, v202 op_sel_hi:[0,0,0]
	s_mov_b32 m0, s20
	v_mfma_scale_f32_16x16x128_f8f6f4 v[156:159], v[2:9], v[26:33], v[156:159], v202, v202 op_sel_hi:[0,0,0]
	global_load_lds_dwordx4 v205, s[26:27]
	v_mfma_scale_f32_16x16x128_f8f6f4 v[152:155], v[10:17], v[26:33], v[152:155], v202, v202 op_sel_hi:[0,0,0]
	v_mfma_scale_f32_16x16x128_f8f6f4 v[148:151], v[2:9], v[34:41], v[148:151], v202, v202 op_sel_hi:[0,0,0]
	s_mov_b32 m0, s21
	v_mfma_scale_f32_16x16x128_f8f6f4 v[144:147], v[10:17], v[34:41], v[188:191], v202, v202 op_sel_hi:[0,0,0]
	global_load_lds_dwordx4 v206, s[26:27]
	v_mfma_scale_f32_16x16x128_f8f6f4 v[136:139], v[2:9], v[42:49], v[192:195], v202, v202 op_sel_hi:[0,0,0]
	v_mfma_scale_f32_16x16x128_f8f6f4 v[132:135], v[10:17], v[42:49], v[196:199], v202, v202 op_sel_hi:[0,0,0]
	s_setprio 0
	s_barrier
	s_add_i32 s26, 0, 0x1c000
	v_add_u32_e32 v0, s26, v207
	ds_read_b128 v[52:55], v0
	ds_read_b128 v[56:59], v0 offset:1024
	ds_read_b128 v[68:71], v0 offset:2048
	ds_read_b128 v[72:75], v0 offset:3072
	s_add_i32 s25, s25, s73
	v_mov_b32_e32 v0, v206
	v_lshl_add_u64 v[50:51], s[6:7], 0, v[0:1]
	v_lshl_add_u64 v[50:51], v[50:51], 0, s[66:67]
	s_barrier
	s_waitcnt lgkmcnt(0)
	s_setprio 1
	s_waitcnt lgkmcnt(0)
	v_mfma_scale_f32_16x16x128_f8f6f4 v[128:131], v[52:59], v[18:25], v[128:131], v202, v202 op_sel_hi:[0,0,0]
	v_mfma_scale_f32_16x16x128_f8f6f4 v[124:127], v[68:75], v[18:25], v[124:127], v202, v202 op_sel_hi:[0,0,0]
	s_add_u32 s98, s6, s66
	s_addc_u32 s99, s7, s67
	s_mov_b32 m0, s25
	v_mfma_scale_f32_16x16x128_f8f6f4 v[120:123], v[52:59], v[26:33], v[120:123], v202, v202 op_sel_hi:[0,0,0]
	global_load_lds_dwordx4 v205, s[98:99]
	v_mfma_scale_f32_16x16x128_f8f6f4 v[116:119], v[68:75], v[26:33], v[116:119], v202, v202 op_sel_hi:[0,0,0]
	v_mfma_scale_f32_16x16x128_f8f6f4 v[112:115], v[52:59], v[34:41], v[210:213], v202, v202 op_sel_hi:[0,0,0]
	s_add_i32 m0, s25, 0x2000
	v_mfma_scale_f32_16x16x128_f8f6f4 v[108:111], v[68:75], v[34:41], v[172:175], v202, v202 op_sel_hi:[0,0,0]
	global_load_lds_dwordx4 v206, s[98:99]
	v_mfma_scale_f32_16x16x128_f8f6f4 v[104:107], v[52:59], v[42:49], v[176:179], v202, v202 op_sel_hi:[0,0,0]
	v_mfma_scale_f32_16x16x128_f8f6f4 v[100:103], v[68:75], v[42:49], v[180:183], v202, v202 op_sel_hi:[0,0,0]
	s_setprio 0
	s_barrier
	ds_read_b128 v[18:21], v208 offset:49152
	ds_read_b128 v[22:25], v208 offset:50176
	ds_read_b128 v[84:87], v208 offset:51200
	ds_read_b128 v[88:91], v208 offset:52224
	ds_read_b128 v[92:95], v208 offset:53248
	ds_read_b128 v[96:99], v208 offset:54272
	ds_read_b128 v[172:175], v208 offset:55296
	ds_read_b128 v[176:179], v208 offset:56320
	v_mov_b32_e32 v0, v206
	v_lshl_add_u64 v[26:27], s[10:11], 0, v[0:1]
	v_lshl_add_u64 v[26:27], v[26:27], 0, s[66:67]
	s_barrier
	s_waitcnt lgkmcnt(0)
	s_setprio 1
	s_waitcnt lgkmcnt(0)
	v_mfma_scale_f32_16x16x128_f8f6f4 v[80:83], v[2:9], v[18:25], v[80:83], v202, v202 op_sel_hi:[0,0,0]
	v_mfma_scale_f32_16x16x128_f8f6f4 v[76:79], v[10:17], v[18:25], v[76:79], v202, v202 op_sel_hi:[0,0,0]
	s_add_u32 s98, s10, s66
	s_addc_u32 s99, s11, s67
	s_mov_b32 m0, s22
	v_mfma_scale_f32_16x16x128_f8f6f4 v[64:67], v[2:9], v[84:91], v[64:67], v202, v202 op_sel_hi:[0,0,0]
	global_load_lds_dwordx4 v205, s[98:99]
	v_mfma_scale_f32_16x16x128_f8f6f4 v[60:63], v[10:17], v[84:91], v[60:63], v202, v202 op_sel_hi:[0,0,0]
	v_mfma_scale_f32_16x16x128_f8f6f4 v[48:51], v[2:9], v[92:99], v[184:187], v202, v202 op_sel_hi:[0,0,0]
	s_mov_b32 m0, s34
	v_mfma_scale_f32_16x16x128_f8f6f4 v[44:47], v[10:17], v[92:99], v[214:217], v202, v202 op_sel_hi:[0,0,0]
	global_load_lds_dwordx4 v206, s[98:99]
	v_mfma_scale_f32_16x16x128_f8f6f4 v[40:43], v[2:9], v[172:179], v[218:221], v202, v202 op_sel_hi:[0,0,0]
	v_mfma_scale_f32_16x16x128_f8f6f4 v[36:39], v[10:17], v[172:179], v[222:225], v202, v202 op_sel_hi:[0,0,0]
	s_setprio 0
	s_barrier
	s_add_u32 s6, s6, 0x40080
	s_addc_u32 s7, s7, 0
	s_add_i32 s10, s26, s73
	s_nop 0
	s_nop 0
	s_waitcnt vmcnt(4)
	s_barrier
	s_setprio 1
	v_mfma_scale_f32_16x16x128_f8f6f4 v[32:35], v[52:59], v[18:25], v[226:229], v202, v202 op_sel_hi:[0,0,0]
	v_mfma_scale_f32_16x16x128_f8f6f4 v[28:31], v[68:75], v[18:25], v[230:233], v202, v202 op_sel_hi:[0,0,0]
	s_mov_b32 m0, s10
	v_mfma_scale_f32_16x16x128_f8f6f4 v[24:27], v[52:59], v[84:91], v[234:237], v202, v202 op_sel_hi:[0,0,0]
	global_load_lds_dwordx4 v205, s[6:7]
	v_mfma_scale_f32_16x16x128_f8f6f4 v[20:23], v[68:75], v[84:91], v[238:241], v202, v202 op_sel_hi:[0,0,0]
	v_mfma_scale_f32_16x16x128_f8f6f4 v[16:19], v[52:59], v[92:99], v[242:245], v202, v202 op_sel_hi:[0,0,0]
	s_add_i32 m0, s10, 0x2000
	v_mfma_scale_f32_16x16x128_f8f6f4 v[12:15], v[68:75], v[92:99], v[246:249], v202, v202 op_sel_hi:[0,0,0]
	global_load_lds_dwordx4 v206, s[6:7]
	v_mfma_scale_f32_16x16x128_f8f6f4 v[8:11], v[52:59], v[172:179], v[168:171], v202, v202 op_sel_hi:[0,0,0]
	v_mfma_scale_f32_16x16x128_f8f6f4 v[4:7], v[68:75], v[172:179], v[140:143], v202, v202 op_sel_hi:[0,0,0]
	s_setprio 0
	s_add_i32 s17, s17, 2
	s_add_u32 s4, s4, 0x100
	s_addc_u32 s5, s5, 0
	s_add_u32 s15, s15, 0x100
	s_addc_u32 s16, s16, 0
	s_cmp_gt_u32 s17, 13
	s_barrier
	s_cbranch_scc0 .LBB0_278

.LBB0_1503:
	s_add_u32 s24, s2, 0xfffc0080
	s_addc_u32 s25, s3, -1
	s_add_i32 s28, 0, 0x10000
	v_add_u32_e32 v128, s28, v150
	ds_read_b128 v[136:139], v128
	ds_read_b128 v[140:143], v128 offset:1024
	ds_read_b128 v[152:155], v128 offset:2048
	ds_read_b128 v[156:159], v128 offset:3072
	s_cmp_eq_u32 s22, 12
	s_cselect_b32 s41, s49, s25
	s_cselect_b32 s40, s48, s24
	s_cselect_b32 s39, s59, s20
	s_cselect_b32 s38, s58, s7
	ds_read_b128 v[160:163], v151
	ds_read_b128 v[164:167], v151 offset:1024
	ds_read_b128 v[168:171], v151 offset:2048
	ds_read_b128 v[172:175], v151 offset:3072
	ds_read_b128 v[176:179], v151 offset:4096
	ds_read_b128 v[180:183], v151 offset:5120
	ds_read_b128 v[184:187], v151 offset:6144
	ds_read_b128 v[188:191], v151 offset:7168
	s_nop 0
	v_mov_b32_e32 v128, v149
	s_nop 0
	s_waitcnt lgkmcnt(8)
	s_barrier
	s_waitcnt lgkmcnt(0)
	s_setprio 1
	s_waitcnt lgkmcnt(0)
	v_mfma_scale_f32_16x16x128_f8f6f4 v[124:127], v[136:143], v[160:167], v[124:127], v146, v146 op_sel_hi:[0,0,0]
	v_mfma_scale_f32_16x16x128_f8f6f4 v[120:123], v[152:159], v[160:167], v[120:123], v146, v146 op_sel_hi:[0,0,0]
	s_add_i32 m0, s0, 0xc000
	v_mfma_scale_f32_16x16x128_f8f6f4 v[116:119], v[136:143], v[168:175], v[116:119], v146, v146 op_sel_hi:[0,0,0]
	global_load_lds_dwordx4 v148, s[2:3]
	v_mfma_scale_f32_16x16x128_f8f6f4 v[112:115], v[152:159], v[168:175], v[112:115], v146, v146 op_sel_hi:[0,0,0]
	v_mfma_scale_f32_16x16x128_f8f6f4 v[128:131], v[136:143], v[176:183], v[108:111], v146, v146 op_sel_hi:[0,0,0]
	s_add_i32 m0, s0, 0xe000
	v_mfma_scale_f32_16x16x128_f8f6f4 v[192:195], v[152:159], v[176:183], v[104:107], v146, v146 op_sel_hi:[0,0,0]
	global_load_lds_dwordx4 v149, s[2:3]
	v_mfma_scale_f32_16x16x128_f8f6f4 v[196:199], v[136:143], v[184:191], v[100:103], v146, v146 op_sel_hi:[0,0,0]
	v_mfma_scale_f32_16x16x128_f8f6f4 v[200:203], v[152:159], v[184:191], v[96:99], v146, v146 op_sel_hi:[0,0,0]
	s_setprio 0
	s_barrier
	s_add_i32 s29, 0, 0x14000
	s_nop 0
	v_add_u32_e32 v108, s29, v150
	s_add_i32 s24, s28, s21
	ds_read_b128 v[96:99], v108
	ds_read_b128 v[100:103], v108 offset:1024
	ds_read_b128 v[104:107], v108 offset:2048
	ds_read_b128 v[108:111], v108 offset:3072
	s_nop 0
	s_nop 0
	s_barrier
	s_waitcnt lgkmcnt(0)
	s_setprio 1
	s_waitcnt lgkmcnt(0)
	v_mfma_scale_f32_16x16x128_f8f6f4 v[204:207], v[96:103], v[160:167], v[60:63], v146, v146 op_sel_hi:[0,0,0]
	v_mfma_scale_f32_16x16x128_f8f6f4 v[160:163], v[104:111], v[160:167], v[56:59], v146, v146 op_sel_hi:[0,0,0]
	s_mov_b32 m0, s24
	v_mfma_scale_f32_16x16x128_f8f6f4 v[164:167], v[96:103], v[168:175], v[52:55], v146, v146 op_sel_hi:[0,0,0]
	global_load_lds_dwordx4 v148, s[38:39]
	v_mfma_scale_f32_16x16x128_f8f6f4 v[168:171], v[104:111], v[168:175], v[48:51], v146, v146 op_sel_hi:[0,0,0]
	v_mfma_scale_f32_16x16x128_f8f6f4 v[172:175], v[96:103], v[176:183], v[44:47], v146, v146 op_sel_hi:[0,0,0]
	s_add_i32 m0, s24, 0x2000
	v_mfma_scale_f32_16x16x128_f8f6f4 v[176:179], v[104:111], v[176:183], v[40:43], v146, v146 op_sel_hi:[0,0,0]
	global_load_lds_dwordx4 v149, s[38:39]
	v_mfma_scale_f32_16x16x128_f8f6f4 v[180:183], v[96:103], v[184:191], v[36:39], v146, v146 op_sel_hi:[0,0,0]
	v_mfma_scale_f32_16x16x128_f8f6f4 v[184:187], v[104:111], v[184:191], v[32:35], v146, v146 op_sel_hi:[0,0,0]
	s_setprio 0
	s_barrier
	s_nop 2
	ds_read_b128 v[32:35], v151 offset:16384
	ds_read_b128 v[36:39], v151 offset:17408
	ds_read_b128 v[40:43], v151 offset:18432
	ds_read_b128 v[44:47], v151 offset:19456
	ds_read_b128 v[48:51], v151 offset:20480
	ds_read_b128 v[52:55], v151 offset:21504
	ds_read_b128 v[56:59], v151 offset:22528
	ds_read_b128 v[60:63], v151 offset:23552
	s_nop 0
	s_nop 0
	s_barrier
	s_waitcnt lgkmcnt(0)
	s_setprio 1
	s_waitcnt lgkmcnt(0)
	v_mfma_scale_f32_16x16x128_f8f6f4 v[92:95], v[136:143], v[32:39], v[92:95], v146, v146 op_sel_hi:[0,0,0]
	v_mfma_scale_f32_16x16x128_f8f6f4 v[88:91], v[152:159], v[32:39], v[88:91], v146, v146 op_sel_hi:[0,0,0]
	s_mov_b32 m0, s0
	v_mfma_scale_f32_16x16x128_f8f6f4 v[84:87], v[136:143], v[40:47], v[84:87], v146, v146 op_sel_hi:[0,0,0]
	global_load_lds_dwordx4 v148, s[40:41]
	v_mfma_scale_f32_16x16x128_f8f6f4 v[80:83], v[152:159], v[40:47], v[80:83], v146, v146 op_sel_hi:[0,0,0]
	v_mfma_scale_f32_16x16x128_f8f6f4 v[76:79], v[136:143], v[48:55], v[76:79], v146, v146 op_sel_hi:[0,0,0]
	s_mov_b32 m0, s1
	v_mfma_scale_f32_16x16x128_f8f6f4 v[72:75], v[152:159], v[48:55], v[72:75], v146, v146 op_sel_hi:[0,0,0]
	global_load_lds_dwordx4 v149, s[40:41]
	v_mfma_scale_f32_16x16x128_f8f6f4 v[188:191], v[136:143], v[56:63], v[68:71], v146, v146 op_sel_hi:[0,0,0]
	v_mfma_scale_f32_16x16x128_f8f6f4 v[208:211], v[152:159], v[56:63], v[64:67], v146, v146 op_sel_hi:[0,0,0]
	s_setprio 0
	s_barrier
	s_add_u32 s24, s38, 0x40000
	s_addc_u32 s25, s39, 0
	s_nop 2
	s_add_i32 s28, s29, s21
	s_mov_b32 s100, s28
	s_nop 0
	s_add_i32 s101, s28, 0x2000
	s_nop 0
	s_waitcnt vmcnt(4)
	s_barrier
	s_setprio 1
	v_mfma_scale_f32_16x16x128_f8f6f4 v[212:215], v[96:103], v[32:39], v[28:31], v146, v146 op_sel_hi:[0,0,0]
	v_mfma_scale_f32_16x16x128_f8f6f4 v[216:219], v[104:111], v[32:39], v[24:27], v146, v146 op_sel_hi:[0,0,0]
	s_mov_b32 m0, s100
	v_mfma_scale_f32_16x16x128_f8f6f4 v[220:223], v[96:103], v[40:47], v[20:23], v146, v146 op_sel_hi:[0,0,0]
	global_load_lds_dwordx4 v148, s[24:25]
	v_mfma_scale_f32_16x16x128_f8f6f4 v[224:227], v[104:111], v[40:47], v[16:19], v146, v146 op_sel_hi:[0,0,0]
	v_mfma_scale_f32_16x16x128_f8f6f4 v[228:231], v[96:103], v[48:55], v[12:15], v146, v146 op_sel_hi:[0,0,0]
	s_mov_b32 m0, s101
	v_mfma_scale_f32_16x16x128_f8f6f4 v[232:235], v[104:111], v[48:55], v[8:11], v146, v146 op_sel_hi:[0,0,0]
	global_load_lds_dwordx4 v149, s[24:25]
	v_mfma_scale_f32_16x16x128_f8f6f4 v[236:239], v[96:103], v[56:63], v[4:7], v146, v146 op_sel_hi:[0,0,0]
	v_mfma_scale_f32_16x16x128_f8f6f4 v[240:243], v[104:111], v[56:63], v[0:3], v146, v146 op_sel_hi:[0,0,0]
	s_setprio 0
	s_add_i32 s28, 0, 0x18000
	s_nop 1
	v_add_u32_e32 v12, s28, v150
	s_barrier
	s_nop 0
	ds_read_b128 v[0:3], v12
	ds_read_b128 v[4:7], v12 offset:1024
	ds_read_b128 v[8:11], v12 offset:2048
	ds_read_b128 v[12:15], v12 offset:3072
	s_add_u32 s24, s40, 0x40000
	ds_read_b128 v[16:19], v151 offset:32768
	ds_read_b128 v[20:23], v151 offset:33792
	ds_read_b128 v[24:27], v151 offset:34816
	ds_read_b128 v[28:31], v151 offset:35840
	ds_read_b128 v[32:35], v151 offset:36864
	ds_read_b128 v[36:39], v151 offset:37888
	ds_read_b128 v[64:67], v151 offset:38912
	ds_read_b128 v[68:71], v151 offset:39936
	s_addc_u32 s25, s41, 0
	s_nop 0
	s_nop 0
	s_waitcnt lgkmcnt(8)
	s_barrier
	s_waitcnt lgkmcnt(0)
	s_setprio 1
	s_waitcnt lgkmcnt(0)
	v_mfma_scale_f32_16x16x128_f8f6f4 v[124:127], v[0:7], v[16:23], v[124:127], v146, v146 op_sel_hi:[0,0,0]
	v_mfma_scale_f32_16x16x128_f8f6f4 v[120:123], v[8:15], v[16:23], v[120:123], v146, v146 op_sel_hi:[0,0,0]
	s_mov_b32 m0, s8
	v_mfma_scale_f32_16x16x128_f8f6f4 v[116:119], v[0:7], v[24:31], v[116:119], v146, v146 op_sel_hi:[0,0,0]
	global_load_lds_dwordx4 v148, s[24:25]
	v_mfma_scale_f32_16x16x128_f8f6f4 v[112:115], v[8:15], v[24:31], v[112:115], v146, v146 op_sel_hi:[0,0,0]
	v_mfma_scale_f32_16x16x128_f8f6f4 v[108:111], v[0:7], v[32:39], v[128:131], v146, v146 op_sel_hi:[0,0,0]
	s_mov_b32 m0, s9
	v_mfma_scale_f32_16x16x128_f8f6f4 v[104:107], v[8:15], v[32:39], v[192:195], v146, v146 op_sel_hi:[0,0,0]
	global_load_lds_dwordx4 v149, s[24:25]
	v_mfma_scale_f32_16x16x128_f8f6f4 v[100:103], v[0:7], v[64:71], v[196:199], v146, v146 op_sel_hi:[0,0,0]
	v_mfma_scale_f32_16x16x128_f8f6f4 v[96:99], v[8:15], v[64:71], v[200:203], v146, v146 op_sel_hi:[0,0,0]
	s_setprio 0
	s_barrier
	s_add_i32 s29, 0, 0x1c000
	v_add_u32_e32 v40, s29, v150
	ds_read_b128 v[136:139], v40
	ds_read_b128 v[140:143], v40 offset:1024
	ds_read_b128 v[152:155], v40 offset:2048
	ds_read_b128 v[156:159], v40 offset:3072
	s_add_i32 s24, s28, s21
	v_mov_b32_e32 v132, v149
	v_lshl_add_u64 v[40:41], s[38:39], 0, v[132:133]
	v_lshl_add_u64 v[40:41], v[40:41], 0, s[52:53]
	s_barrier
	s_waitcnt lgkmcnt(0)
	s_setprio 1
	s_waitcnt lgkmcnt(0)
	v_mfma_scale_f32_16x16x128_f8f6f4 v[60:63], v[136:143], v[16:23], v[204:207], v146, v146 op_sel_hi:[0,0,0]
	v_mfma_scale_f32_16x16x128_f8f6f4 v[56:59], v[152:159], v[16:23], v[160:163], v146, v146 op_sel_hi:[0,0,0]
	s_add_u32 s98, s38, s52
	s_addc_u32 s99, s39, s53
	s_mov_b32 m0, s24
	v_mfma_scale_f32_16x16x128_f8f6f4 v[52:55], v[136:143], v[24:31], v[164:167], v146, v146 op_sel_hi:[0,0,0]
	global_load_lds_dwordx4 v148, s[98:99]
	v_mfma_scale_f32_16x16x128_f8f6f4 v[48:51], v[152:159], v[24:31], v[168:171], v146, v146 op_sel_hi:[0,0,0]
	v_mfma_scale_f32_16x16x128_f8f6f4 v[44:47], v[136:143], v[32:39], v[172:175], v146, v146 op_sel_hi:[0,0,0]
	s_add_i32 m0, s24, 0x2000
	v_mfma_scale_f32_16x16x128_f8f6f4 v[40:43], v[152:159], v[32:39], v[176:179], v146, v146 op_sel_hi:[0,0,0]
	global_load_lds_dwordx4 v149, s[98:99]
	v_mfma_scale_f32_16x16x128_f8f6f4 v[36:39], v[136:143], v[64:71], v[180:183], v146, v146 op_sel_hi:[0,0,0]
	v_mfma_scale_f32_16x16x128_f8f6f4 v[32:35], v[152:159], v[64:71], v[184:187], v146, v146 op_sel_hi:[0,0,0]
	s_setprio 0
	s_barrier
	ds_read_b128 v[16:19], v151 offset:49152
	ds_read_b128 v[20:23], v151 offset:50176
	ds_read_b128 v[160:163], v151 offset:51200
	ds_read_b128 v[164:167], v151 offset:52224
	ds_read_b128 v[168:171], v151 offset:53248
	ds_read_b128 v[172:175], v151 offset:54272
	ds_read_b128 v[176:179], v151 offset:55296
	ds_read_b128 v[180:183], v151 offset:56320
	v_mov_b32_e32 v132, v149
	v_lshl_add_u64 v[24:25], s[40:41], 0, v[132:133]
	v_lshl_add_u64 v[24:25], v[24:25], 0, s[52:53]
	s_barrier
	s_waitcnt lgkmcnt(0)
	s_setprio 1
	s_waitcnt lgkmcnt(0)
	v_mfma_scale_f32_16x16x128_f8f6f4 v[92:95], v[0:7], v[16:23], v[92:95], v146, v146 op_sel_hi:[0,0,0]
	v_mfma_scale_f32_16x16x128_f8f6f4 v[88:91], v[8:15], v[16:23], v[88:91], v146, v146 op_sel_hi:[0,0,0]
	s_add_u32 s98, s40, s52
	s_addc_u32 s99, s41, s53
	s_mov_b32 m0, s10
	v_mfma_scale_f32_16x16x128_f8f6f4 v[84:87], v[0:7], v[160:167], v[84:87], v146, v146 op_sel_hi:[0,0,0]
	global_load_lds_dwordx4 v148, s[98:99]
	v_mfma_scale_f32_16x16x128_f8f6f4 v[80:83], v[8:15], v[160:167], v[80:83], v146, v146 op_sel_hi:[0,0,0]
	v_mfma_scale_f32_16x16x128_f8f6f4 v[76:79], v[0:7], v[168:175], v[76:79], v146, v146 op_sel_hi:[0,0,0]
	s_mov_b32 m0, s11
	v_mfma_scale_f32_16x16x128_f8f6f4 v[72:75], v[8:15], v[168:175], v[72:75], v146, v146 op_sel_hi:[0,0,0]
	global_load_lds_dwordx4 v149, s[98:99]
	v_mfma_scale_f32_16x16x128_f8f6f4 v[68:71], v[0:7], v[176:183], v[188:191], v146, v146 op_sel_hi:[0,0,0]
	v_mfma_scale_f32_16x16x128_f8f6f4 v[64:67], v[8:15], v[176:183], v[208:211], v146, v146 op_sel_hi:[0,0,0]
	s_setprio 0
	s_barrier
	s_add_u32 s24, s38, 0x40080
	s_addc_u32 s25, s39, 0
	s_add_i32 s28, s29, s21
	s_nop 0
	v_mov_b32_e32 v0, v149
	s_nop 0
	s_waitcnt vmcnt(4)
	s_barrier
	s_setprio 1
	v_mfma_scale_f32_16x16x128_f8f6f4 v[28:31], v[136:143], v[16:23], v[212:215], v146, v146 op_sel_hi:[0,0,0]
	v_mfma_scale_f32_16x16x128_f8f6f4 v[24:27], v[152:159], v[16:23], v[216:219], v146, v146 op_sel_hi:[0,0,0]
	s_mov_b32 m0, s28
	v_mfma_scale_f32_16x16x128_f8f6f4 v[20:23], v[136:143], v[160:167], v[220:223], v146, v146 op_sel_hi:[0,0,0]
	global_load_lds_dwordx4 v148, s[24:25]
	v_mfma_scale_f32_16x16x128_f8f6f4 v[16:19], v[152:159], v[160:167], v[224:227], v146, v146 op_sel_hi:[0,0,0]
	v_mfma_scale_f32_16x16x128_f8f6f4 v[12:15], v[136:143], v[168:175], v[228:231], v146, v146 op_sel_hi:[0,0,0]
	s_add_i32 m0, s28, 0x2000
	v_mfma_scale_f32_16x16x128_f8f6f4 v[8:11], v[152:159], v[168:175], v[232:235], v146, v146 op_sel_hi:[0,0,0]
	global_load_lds_dwordx4 v149, s[24:25]
	v_mfma_scale_f32_16x16x128_f8f6f4 v[4:7], v[136:143], v[176:183], v[236:239], v146, v146 op_sel_hi:[0,0,0]
	v_mfma_scale_f32_16x16x128_f8f6f4 v[0:3], v[152:159], v[176:183], v[240:243], v146, v146 op_sel_hi:[0,0,0]
	s_setprio 0
	s_add_i32 s22, s22, 2
	s_add_u32 s2, s2, 0x100
	s_addc_u32 s3, s3, 0
	s_add_u32 s7, s7, 0x100
	s_addc_u32 s20, s20, 0
	s_cmp_gt_u32 s22, 13
	s_barrier
	s_cbranch_scc0 .LBB0_1503

.LBB0_2382:
	ds_read_b128 v[140:143], v134
	ds_read_b128 v[144:147], v134 offset:1024
	ds_read_b128 v[148:151], v134 offset:2048
	ds_read_b128 v[152:155], v134 offset:3072
	s_add_u32 s18, s16, 0xfffd0080
	s_addc_u32 s19, s17, -1
	s_cmp_eq_u32 s54, 8
	s_cselect_b32 s21, s15, s19
	s_cselect_b32 s20, s14, s18
	s_cselect_b32 s19, s13, s53
	s_cselect_b32 s18, s12, s52
	ds_read_b128 v[156:159], v135
	ds_read_b128 v[160:163], v135 offset:1024
	ds_read_b128 v[164:167], v135 offset:2048
	ds_read_b128 v[168:171], v135 offset:3072
	ds_read_b128 v[172:175], v135 offset:4096
	ds_read_b128 v[176:179], v135 offset:5120
	ds_read_b128 v[180:183], v135 offset:6144
	ds_read_b128 v[184:187], v135 offset:7168
	s_nop 0
	s_nop 0
	s_waitcnt lgkmcnt(8)
	s_barrier
	s_waitcnt lgkmcnt(0)
	s_setprio 1
	s_waitcnt lgkmcnt(0)
	v_mfma_scale_f32_16x16x128_f8f6f4 v[124:127], v[140:147], v[156:163], v[124:127], v136, v136 op_sel_hi:[0,0,0]
	v_mfma_scale_f32_16x16x128_f8f6f4 v[120:123], v[148:155], v[156:163], v[120:123], v136, v136 op_sel_hi:[0,0,0]
	s_mov_b32 m0, s39
	v_mfma_scale_f32_16x16x128_f8f6f4 v[116:119], v[140:147], v[164:171], v[116:119], v136, v136 op_sel_hi:[0,0,0]
	global_load_lds_dwordx4 v132, s[16:17]
	v_mfma_scale_f32_16x16x128_f8f6f4 v[112:115], v[148:155], v[164:171], v[112:115], v136, v136 op_sel_hi:[0,0,0]
	v_mfma_scale_f32_16x16x128_f8f6f4 v[188:191], v[140:147], v[172:179], v[108:111], v136, v136 op_sel_hi:[0,0,0]
	s_mov_b32 m0, s40
	v_mfma_scale_f32_16x16x128_f8f6f4 v[192:195], v[148:155], v[172:179], v[104:107], v136, v136 op_sel_hi:[0,0,0]
	global_load_lds_dwordx4 v133, s[16:17]
	v_mfma_scale_f32_16x16x128_f8f6f4 v[196:199], v[140:147], v[180:187], v[100:103], v136, v136 op_sel_hi:[0,0,0]
	v_mfma_scale_f32_16x16x128_f8f6f4 v[200:203], v[148:155], v[180:187], v[96:99], v136, v136 op_sel_hi:[0,0,0]
	s_setprio 0
	s_barrier
	s_nop 2
	ds_read_b128 v[96:99], v137
	ds_read_b128 v[100:103], v137 offset:1024
	ds_read_b128 v[104:107], v137 offset:2048
	ds_read_b128 v[108:111], v137 offset:3072
	s_nop 0
	s_nop 0
	s_barrier
	s_waitcnt lgkmcnt(0)
	s_setprio 1
	s_waitcnt lgkmcnt(0)
	v_mfma_scale_f32_16x16x128_f8f6f4 v[204:207], v[96:103], v[156:163], v[92:95], v136, v136 op_sel_hi:[0,0,0]
	v_mfma_scale_f32_16x16x128_f8f6f4 v[156:159], v[104:111], v[156:163], v[88:91], v136, v136 op_sel_hi:[0,0,0]
	s_mov_b32 m0, s41
	v_mfma_scale_f32_16x16x128_f8f6f4 v[160:163], v[96:103], v[164:171], v[84:87], v136, v136 op_sel_hi:[0,0,0]
	global_load_lds_dwordx4 v132, s[18:19]
	v_mfma_scale_f32_16x16x128_f8f6f4 v[164:167], v[104:111], v[164:171], v[80:83], v136, v136 op_sel_hi:[0,0,0]
	v_mfma_scale_f32_16x16x128_f8f6f4 v[168:171], v[96:103], v[172:179], v[76:79], v136, v136 op_sel_hi:[0,0,0]
	s_mov_b32 m0, s42
	v_mfma_scale_f32_16x16x128_f8f6f4 v[172:175], v[104:111], v[172:179], v[72:75], v136, v136 op_sel_hi:[0,0,0]
	global_load_lds_dwordx4 v133, s[18:19]
	v_mfma_scale_f32_16x16x128_f8f6f4 v[176:179], v[96:103], v[180:187], v[68:71], v136, v136 op_sel_hi:[0,0,0]
	v_mfma_scale_f32_16x16x128_f8f6f4 v[180:183], v[104:111], v[180:187], v[64:67], v136, v136 op_sel_hi:[0,0,0]
	s_setprio 0
	s_barrier
	s_nop 2
	ds_read_b128 v[64:67], v135 offset:16384
	ds_read_b128 v[68:71], v135 offset:17408
	ds_read_b128 v[72:75], v135 offset:18432
	ds_read_b128 v[76:79], v135 offset:19456
	ds_read_b128 v[80:83], v135 offset:20480
	ds_read_b128 v[84:87], v135 offset:21504
	ds_read_b128 v[88:91], v135 offset:22528
	ds_read_b128 v[92:95], v135 offset:23552
	s_nop 0
	s_nop 0
	s_barrier
	s_waitcnt lgkmcnt(0)
	s_setprio 1
	s_waitcnt lgkmcnt(0)
	v_mfma_scale_f32_16x16x128_f8f6f4 v[60:63], v[140:147], v[64:71], v[60:63], v136, v136 op_sel_hi:[0,0,0]
	v_mfma_scale_f32_16x16x128_f8f6f4 v[56:59], v[148:155], v[64:71], v[56:59], v136, v136 op_sel_hi:[0,0,0]
	s_mov_b32 m0, s25
	v_mfma_scale_f32_16x16x128_f8f6f4 v[52:55], v[140:147], v[72:79], v[52:55], v136, v136 op_sel_hi:[0,0,0]
	global_load_lds_dwordx4 v132, s[20:21]
	v_mfma_scale_f32_16x16x128_f8f6f4 v[48:51], v[148:155], v[72:79], v[48:51], v136, v136 op_sel_hi:[0,0,0]
	v_mfma_scale_f32_16x16x128_f8f6f4 v[184:187], v[140:147], v[80:87], v[44:47], v136, v136 op_sel_hi:[0,0,0]
	s_mov_b32 m0, s26
	v_mfma_scale_f32_16x16x128_f8f6f4 v[208:211], v[148:155], v[80:87], v[40:43], v136, v136 op_sel_hi:[0,0,0]
	global_load_lds_dwordx4 v133, s[20:21]
	v_mfma_scale_f32_16x16x128_f8f6f4 v[212:215], v[140:147], v[88:95], v[36:39], v136, v136 op_sel_hi:[0,0,0]
	v_mfma_scale_f32_16x16x128_f8f6f4 v[216:219], v[148:155], v[88:95], v[32:35], v136, v136 op_sel_hi:[0,0,0]
	s_setprio 0
	s_barrier
	s_add_u32 s56, s18, 0x30000
	s_nop 3
	s_addc_u32 s57, s19, 0
	s_nop 0
	s_nop 0
	s_waitcnt vmcnt(4)
	s_barrier
	s_setprio 1
	v_mfma_scale_f32_16x16x128_f8f6f4 v[220:223], v[96:103], v[64:71], v[28:31], v136, v136 op_sel_hi:[0,0,0]
	v_mfma_scale_f32_16x16x128_f8f6f4 v[224:227], v[104:111], v[64:71], v[24:27], v136, v136 op_sel_hi:[0,0,0]
	s_mov_b32 m0, s43
	v_mfma_scale_f32_16x16x128_f8f6f4 v[228:231], v[96:103], v[72:79], v[20:23], v136, v136 op_sel_hi:[0,0,0]
	global_load_lds_dwordx4 v132, s[56:57]
	v_mfma_scale_f32_16x16x128_f8f6f4 v[232:235], v[104:111], v[72:79], v[16:19], v136, v136 op_sel_hi:[0,0,0]
	v_mfma_scale_f32_16x16x128_f8f6f4 v[236:239], v[96:103], v[80:87], v[12:15], v136, v136 op_sel_hi:[0,0,0]
	s_mov_b32 m0, s44
	v_mfma_scale_f32_16x16x128_f8f6f4 v[240:243], v[104:111], v[80:87], v[8:11], v136, v136 op_sel_hi:[0,0,0]
	global_load_lds_dwordx4 v133, s[56:57]
	v_mfma_scale_f32_16x16x128_f8f6f4 v[244:247], v[96:103], v[88:95], v[4:7], v136, v136 op_sel_hi:[0,0,0]
	v_mfma_scale_f32_16x16x128_f8f6f4 v[248:251], v[104:111], v[88:95], v[0:3], v136, v136 op_sel_hi:[0,0,0]
	s_setprio 0
	s_barrier
	s_nop 4
	ds_read_b128 v[0:3], v138
	ds_read_b128 v[4:7], v138 offset:1024
	ds_read_b128 v[8:11], v138 offset:2048
	ds_read_b128 v[12:15], v138 offset:3072
	s_add_u32 s56, s20, 0x30000
	ds_read_b128 v[16:19], v135 offset:32768
	ds_read_b128 v[20:23], v135 offset:33792
	ds_read_b128 v[24:27], v135 offset:34816
	ds_read_b128 v[28:31], v135 offset:35840
	ds_read_b128 v[32:35], v135 offset:36864
	ds_read_b128 v[36:39], v135 offset:37888
	ds_read_b128 v[40:43], v135 offset:38912
	ds_read_b128 v[44:47], v135 offset:39936
	s_addc_u32 s57, s21, 0
	s_nop 0
	s_nop 0
	s_waitcnt lgkmcnt(8)
	s_barrier
	s_waitcnt lgkmcnt(0)
	s_setprio 1
	s_waitcnt lgkmcnt(0)
	v_mfma_scale_f32_16x16x128_f8f6f4 v[124:127], v[0:7], v[16:23], v[124:127], v136, v136 op_sel_hi:[0,0,0]
	v_mfma_scale_f32_16x16x128_f8f6f4 v[120:123], v[8:15], v[16:23], v[120:123], v136, v136 op_sel_hi:[0,0,0]
	s_mov_b32 m0, s27
	v_mfma_scale_f32_16x16x128_f8f6f4 v[116:119], v[0:7], v[24:31], v[116:119], v136, v136 op_sel_hi:[0,0,0]
	global_load_lds_dwordx4 v132, s[56:57]
	v_mfma_scale_f32_16x16x128_f8f6f4 v[112:115], v[8:15], v[24:31], v[112:115], v136, v136 op_sel_hi:[0,0,0]
	v_mfma_scale_f32_16x16x128_f8f6f4 v[108:111], v[0:7], v[32:39], v[188:191], v136, v136 op_sel_hi:[0,0,0]
	s_mov_b32 m0, s28
	v_mfma_scale_f32_16x16x128_f8f6f4 v[104:107], v[8:15], v[32:39], v[192:195], v136, v136 op_sel_hi:[0,0,0]
	global_load_lds_dwordx4 v133, s[56:57]
	v_mfma_scale_f32_16x16x128_f8f6f4 v[100:103], v[0:7], v[40:47], v[196:199], v136, v136 op_sel_hi:[0,0,0]
	v_mfma_scale_f32_16x16x128_f8f6f4 v[96:99], v[8:15], v[40:47], v[200:203], v136, v136 op_sel_hi:[0,0,0]
	s_setprio 0
	s_barrier
	ds_read_b128 v[140:143], v139
	ds_read_b128 v[144:147], v139 offset:1024
	ds_read_b128 v[148:151], v139 offset:2048
	ds_read_b128 v[152:155], v139 offset:3072
	v_mov_b32_e32 v128, v133
	v_lshl_add_u64 v[64:65], s[18:19], 0, v[128:129]
	v_lshl_add_u64 v[64:65], v[64:65], 0, s[4:5]
	s_barrier
	s_waitcnt lgkmcnt(0)
	s_setprio 1
	s_waitcnt lgkmcnt(0)
	v_mfma_scale_f32_16x16x128_f8f6f4 v[92:95], v[140:147], v[16:23], v[204:207], v136, v136 op_sel_hi:[0,0,0]
	v_mfma_scale_f32_16x16x128_f8f6f4 v[88:91], v[148:155], v[16:23], v[156:159], v136, v136 op_sel_hi:[0,0,0]
	s_add_u32 s98, s18, s4
	s_addc_u32 s99, s19, s5
	s_mov_b32 m0, s46
	v_mfma_scale_f32_16x16x128_f8f6f4 v[84:87], v[140:147], v[24:31], v[160:163], v136, v136 op_sel_hi:[0,0,0]
	global_load_lds_dwordx4 v132, s[98:99]
	v_mfma_scale_f32_16x16x128_f8f6f4 v[80:83], v[148:155], v[24:31], v[164:167], v136, v136 op_sel_hi:[0,0,0]
	v_mfma_scale_f32_16x16x128_f8f6f4 v[76:79], v[140:147], v[32:39], v[168:171], v136, v136 op_sel_hi:[0,0,0]
	s_mov_b32 m0, s47
	v_mfma_scale_f32_16x16x128_f8f6f4 v[72:75], v[148:155], v[32:39], v[172:175], v136, v136 op_sel_hi:[0,0,0]
	global_load_lds_dwordx4 v133, s[98:99]
	v_mfma_scale_f32_16x16x128_f8f6f4 v[68:71], v[140:147], v[40:47], v[176:179], v136, v136 op_sel_hi:[0,0,0]
	v_mfma_scale_f32_16x16x128_f8f6f4 v[64:67], v[148:155], v[40:47], v[180:183], v136, v136 op_sel_hi:[0,0,0]
	s_setprio 0
	s_barrier
	ds_read_b128 v[16:19], v135 offset:49152
	ds_read_b128 v[20:23], v135 offset:50176
	ds_read_b128 v[156:159], v135 offset:51200
	ds_read_b128 v[160:163], v135 offset:52224
	ds_read_b128 v[164:167], v135 offset:53248
	ds_read_b128 v[168:171], v135 offset:54272
	ds_read_b128 v[172:175], v135 offset:55296
	ds_read_b128 v[176:179], v135 offset:56320
	v_mov_b32_e32 v128, v133
	v_lshl_add_u64 v[24:25], s[20:21], 0, v[128:129]
	v_lshl_add_u64 v[24:25], v[24:25], 0, s[4:5]
	s_barrier
	s_waitcnt lgkmcnt(0)
	s_setprio 1
	s_waitcnt lgkmcnt(0)
	v_mfma_scale_f32_16x16x128_f8f6f4 v[60:63], v[0:7], v[16:23], v[60:63], v136, v136 op_sel_hi:[0,0,0]
	v_mfma_scale_f32_16x16x128_f8f6f4 v[56:59], v[8:15], v[16:23], v[56:59], v136, v136 op_sel_hi:[0,0,0]
	s_add_u32 s98, s20, s4
	s_addc_u32 s99, s21, s5
	s_mov_b32 m0, s36
	v_mfma_scale_f32_16x16x128_f8f6f4 v[52:55], v[0:7], v[156:163], v[52:55], v136, v136 op_sel_hi:[0,0,0]
	global_load_lds_dwordx4 v132, s[98:99]
	v_mfma_scale_f32_16x16x128_f8f6f4 v[48:51], v[8:15], v[156:163], v[48:51], v136, v136 op_sel_hi:[0,0,0]
	v_mfma_scale_f32_16x16x128_f8f6f4 v[44:47], v[0:7], v[164:171], v[184:187], v136, v136 op_sel_hi:[0,0,0]
	s_mov_b32 m0, s37
	v_mfma_scale_f32_16x16x128_f8f6f4 v[40:43], v[8:15], v[164:171], v[208:211], v136, v136 op_sel_hi:[0,0,0]
	global_load_lds_dwordx4 v133, s[98:99]
	v_mfma_scale_f32_16x16x128_f8f6f4 v[36:39], v[0:7], v[172:179], v[212:215], v136, v136 op_sel_hi:[0,0,0]
	v_mfma_scale_f32_16x16x128_f8f6f4 v[32:35], v[8:15], v[172:179], v[216:219], v136, v136 op_sel_hi:[0,0,0]
	s_setprio 0
	s_barrier
	s_add_u32 s18, s18, 0x30080
	s_addc_u32 s19, s19, 0
	s_add_i32 s20, s45, s24
	s_nop 0
	v_mov_b32_e32 v0, v133
	s_nop 0
	s_waitcnt vmcnt(4)
	s_barrier
	s_setprio 1
	v_mfma_scale_f32_16x16x128_f8f6f4 v[28:31], v[140:147], v[16:23], v[220:223], v136, v136 op_sel_hi:[0,0,0]
	v_mfma_scale_f32_16x16x128_f8f6f4 v[24:27], v[148:155], v[16:23], v[224:227], v136, v136 op_sel_hi:[0,0,0]
	s_mov_b32 m0, s20
	v_mfma_scale_f32_16x16x128_f8f6f4 v[20:23], v[140:147], v[156:163], v[228:231], v136, v136 op_sel_hi:[0,0,0]
	global_load_lds_dwordx4 v132, s[18:19]
	v_mfma_scale_f32_16x16x128_f8f6f4 v[16:19], v[148:155], v[156:163], v[232:235], v136, v136 op_sel_hi:[0,0,0]
	v_mfma_scale_f32_16x16x128_f8f6f4 v[12:15], v[140:147], v[164:171], v[236:239], v136, v136 op_sel_hi:[0,0,0]
	s_add_i32 m0, s20, 0x2000
	v_mfma_scale_f32_16x16x128_f8f6f4 v[8:11], v[148:155], v[164:171], v[240:243], v136, v136 op_sel_hi:[0,0,0]
	global_load_lds_dwordx4 v133, s[18:19]
	v_mfma_scale_f32_16x16x128_f8f6f4 v[4:7], v[140:147], v[172:179], v[244:247], v136, v136 op_sel_hi:[0,0,0]
	v_mfma_scale_f32_16x16x128_f8f6f4 v[0:3], v[148:155], v[172:179], v[248:251], v136, v136 op_sel_hi:[0,0,0]
	s_setprio 0
	s_add_i32 s54, s54, 2
	s_add_u32 s16, s16, 0x100
	s_addc_u32 s17, s17, 0
	s_add_u32 s52, s52, 0x100
	s_addc_u32 s53, s53, 0
	s_cmp_gt_u32 s54, 9
	s_barrier
	s_cbranch_scc0 .LBB0_2382

.LBB0_3995:
	s_add_i32 s34, s6, 2
	s_add_u32 s8, s4, 0xfffe0080
	s_addc_u32 s7, s5, -1
	s_add_i32 s30, 0, 0x10000
	v_add_u32_e32 v140, s30, v200
	ds_read_b128 v[128:131], v140
	ds_read_b128 v[132:135], v140 offset:1024
	ds_read_b128 v[136:139], v140 offset:2048
	ds_read_b128 v[140:143], v140 offset:3072
	s_cmp_eq_u32 s12, s6
	s_cselect_b32 s6, s52, s8
	s_cselect_b32 s7, s53, s7
	s_cselect_b32 s9, s55, s27
	s_cselect_b32 s8, s54, s25
	ds_read_b128 v[144:147], v182
	ds_read_b128 v[148:151], v182 offset:1024
	ds_read_b128 v[152:155], v182 offset:2048
	ds_read_b128 v[156:159], v182 offset:3072
	ds_read_b128 v[160:163], v182 offset:4096
	ds_read_b128 v[164:167], v182 offset:5120
	ds_read_b128 v[184:187], v182 offset:6144
	ds_read_b128 v[188:191], v182 offset:7168
	s_nop 0
	s_nop 0
	s_waitcnt lgkmcnt(8)
	s_barrier
	s_waitcnt lgkmcnt(0)
	s_setprio 1
	s_waitcnt lgkmcnt(0)
	v_mfma_scale_f32_16x16x128_f8f6f4 v[120:123], v[128:135], v[144:151], v[120:123], v183, v183 op_sel_hi:[0,0,0]
	v_mov_b32_e32 v170, v200
	v_mfma_scale_f32_16x16x128_f8f6f4 v[124:127], v[136:143], v[144:151], v[124:127], v183, v183 op_sel_hi:[0,0,0]
	s_add_i32 m0, s3, 0xc000
	v_mfma_scale_f32_16x16x128_f8f6f4 v[200:203], v[136:143], v[160:167], v[88:91], v183, v183 op_sel_hi:[0,0,0]
	global_load_lds_dwordx4 v169, s[4:5]
	v_mfma_scale_f32_16x16x128_f8f6f4 v[176:179], v[128:135], v[152:159], v[108:111], v183, v183 op_sel_hi:[0,0,0]
	v_mfma_scale_f32_16x16x128_f8f6f4 v[192:195], v[136:143], v[152:159], v[104:107], v183, v183 op_sel_hi:[0,0,0]
	s_add_i32 m0, s3, 0xe000
	v_mfma_scale_f32_16x16x128_f8f6f4 v[196:199], v[128:135], v[160:167], v[92:95], v183, v183 op_sel_hi:[0,0,0]
	global_load_lds_dwordx4 v181, s[4:5]
	v_mfma_scale_f32_16x16x128_f8f6f4 v[204:207], v[128:135], v[184:191], v[76:79], v183, v183 op_sel_hi:[0,0,0]
	v_mfma_scale_f32_16x16x128_f8f6f4 v[208:211], v[136:143], v[184:191], v[72:75], v183, v183 op_sel_hi:[0,0,0]
	s_setprio 0
	s_barrier
	s_add_i32 s35, 0, 0x14000
	s_nop 1
	v_add_u32_e32 v92, s35, v170
	v_mov_b32_e32 v104, v180
	s_add_i32 s30, s30, s33
	ds_read_b128 v[72:75], v92
	ds_read_b128 v[76:79], v92 offset:1024
	ds_read_b128 v[88:91], v92 offset:2048
	ds_read_b128 v[92:95], v92 offset:3072
	s_mov_b32 m0, s30
	s_nop 0
	global_load_lds_dwordx4 v104, s[8:9]
	v_mov_b32_e32 v104, v212
	s_add_i32 m0, s30, 0x2000
	s_nop 0
	global_load_lds_dwordx4 v104, s[8:9]
	s_barrier
	s_waitcnt lgkmcnt(0)
	s_setprio 1
	s_waitcnt lgkmcnt(0)
	v_mfma_scale_f32_16x16x128_f8f6f4 v[116:119], v[144:151], v[72:79], v[116:119], v183, v183 op_sel_hi:[0,0,0]
	v_mov_b32_e32 v168, v212
	v_mfma_scale_f32_16x16x128_f8f6f4 v[112:115], v[144:151], v[88:95], v[112:115], v183, v183 op_sel_hi:[0,0,0]
	v_mfma_scale_f32_16x16x128_f8f6f4 v[212:215], v[152:159], v[72:79], v[100:103], v183, v183 op_sel_hi:[0,0,0]
	v_mfma_scale_f32_16x16x128_f8f6f4 v[216:219], v[152:159], v[88:95], v[96:99], v183, v183 op_sel_hi:[0,0,0]
	v_mfma_scale_f32_16x16x128_f8f6f4 v[220:223], v[160:167], v[72:79], v[84:87], v183, v183 op_sel_hi:[0,0,0]
	v_mfma_scale_f32_16x16x128_f8f6f4 v[160:163], v[160:167], v[88:95], v[80:83], v183, v183 op_sel_hi:[0,0,0]
	v_mfma_scale_f32_16x16x128_f8f6f4 v[164:167], v[184:191], v[72:79], v[68:71], v183, v183 op_sel_hi:[0,0,0]
	v_mfma_scale_f32_16x16x128_f8f6f4 v[184:187], v[184:191], v[88:95], v[64:67], v183, v183 op_sel_hi:[0,0,0]
	s_setprio 0
	s_barrier
	s_nop 2
	ds_read_b128 v[64:67], v182 offset:16384
	ds_read_b128 v[68:71], v182 offset:17408
	ds_read_b128 v[80:83], v182 offset:18432
	ds_read_b128 v[84:87], v182 offset:19456
	ds_read_b128 v[96:99], v182 offset:20480
	ds_read_b128 v[100:103], v182 offset:21504
	ds_read_b128 v[104:107], v182 offset:22528
	ds_read_b128 v[108:111], v182 offset:23552
	s_nop 0
	s_nop 0
	s_barrier
	s_waitcnt lgkmcnt(0)
	s_setprio 1
	s_waitcnt lgkmcnt(0)
	v_mfma_scale_f32_16x16x128_f8f6f4 v[224:227], v[128:135], v[64:71], v[60:63], v183, v183 op_sel_hi:[0,0,0]
	v_mfma_scale_f32_16x16x128_f8f6f4 v[228:231], v[136:143], v[64:71], v[56:59], v183, v183 op_sel_hi:[0,0,0]
	s_mov_b32 m0, s3
	v_mfma_scale_f32_16x16x128_f8f6f4 v[232:235], v[128:135], v[80:87], v[44:47], v183, v183 op_sel_hi:[0,0,0]
	global_load_lds_dwordx4 v169, s[6:7]
	v_mfma_scale_f32_16x16x128_f8f6f4 v[236:239], v[136:143], v[80:87], v[40:43], v183, v183 op_sel_hi:[0,0,0]
	v_mfma_scale_f32_16x16x128_f8f6f4 v[240:243], v[128:135], v[96:103], v[28:31], v183, v183 op_sel_hi:[0,0,0]
	s_mov_b32 m0, s11
	v_mfma_scale_f32_16x16x128_f8f6f4 v[244:247], v[136:143], v[96:103], v[24:27], v183, v183 op_sel_hi:[0,0,0]
	global_load_lds_dwordx4 v181, s[6:7]
	v_mfma_scale_f32_16x16x128_f8f6f4 v[248:251], v[128:135], v[104:111], v[12:15], v183, v183 op_sel_hi:[0,0,0]
	v_mfma_scale_f32_16x16x128_f8f6f4 v[172:175], v[136:143], v[104:111], v[8:11], v183, v183 op_sel_hi:[0,0,0]
	s_setprio 0
	s_barrier
	s_add_u32 s30, s8, s20
	s_addc_u32 s31, s9, s21
	s_nop 2
	s_add_i32 s35, s35, s33
	s_mov_b32 s100, s35
	s_nop 0
	s_add_i32 s101, s35, 0x2000
	s_nop 0
	s_waitcnt vmcnt(4)
	s_barrier
	s_setprio 1
	v_mfma_scale_f32_16x16x128_f8f6f4 v[52:55], v[64:71], v[72:79], v[52:55], v183, v183 op_sel_hi:[0,0,0]
	v_mfma_scale_f32_16x16x128_f8f6f4 v[48:51], v[64:71], v[88:95], v[48:51], v183, v183 op_sel_hi:[0,0,0]
	s_mov_b32 m0, s100
	v_mfma_scale_f32_16x16x128_f8f6f4 v[36:39], v[80:87], v[72:79], v[36:39], v183, v183 op_sel_hi:[0,0,0]
	global_load_lds_dwordx4 v180, s[30:31]
	v_mfma_scale_f32_16x16x128_f8f6f4 v[32:35], v[80:87], v[88:95], v[32:35], v183, v183 op_sel_hi:[0,0,0]
	v_mfma_scale_f32_16x16x128_f8f6f4 v[20:23], v[96:103], v[72:79], v[20:23], v183, v183 op_sel_hi:[0,0,0]
	s_mov_b32 m0, s101
	v_mfma_scale_f32_16x16x128_f8f6f4 v[16:19], v[96:103], v[88:95], v[16:19], v183, v183 op_sel_hi:[0,0,0]
	global_load_lds_dwordx4 v168, s[30:31]
	v_mfma_scale_f32_16x16x128_f8f6f4 v[4:7], v[104:111], v[72:79], v[4:7], v183, v183 op_sel_hi:[0,0,0]
	v_mfma_scale_f32_16x16x128_f8f6f4 v[0:3], v[104:111], v[88:95], v[0:3], v183, v183 op_sel_hi:[0,0,0]
	s_setprio 0
	s_add_i32 s35, 0, 0x18000
	v_add_u32_e32 v24, s35, v170
	s_barrier
	ds_read_b128 v[8:11], v24
	ds_read_b128 v[12:15], v24 offset:1024
	ds_read_b128 v[128:131], v24 offset:2048
	ds_read_b128 v[132:135], v24 offset:3072
	s_add_u32 s36, s6, 0x20000
	ds_read_b128 v[24:27], v182 offset:32768
	ds_read_b128 v[28:31], v182 offset:33792
	ds_read_b128 v[40:43], v182 offset:34816
	ds_read_b128 v[44:47], v182 offset:35840
	ds_read_b128 v[56:59], v182 offset:36864
	ds_read_b128 v[60:63], v182 offset:37888
	ds_read_b128 v[136:139], v182 offset:38912
	ds_read_b128 v[140:143], v182 offset:39936
	s_addc_u32 s37, s7, 0
	s_nop 0
	s_nop 0
	s_waitcnt lgkmcnt(8)
	s_barrier
	s_waitcnt lgkmcnt(0)
	s_setprio 1
	s_waitcnt lgkmcnt(0)
	v_mfma_scale_f32_16x16x128_f8f6f4 v[120:123], v[8:15], v[24:31], v[120:123], v183, v183 op_sel_hi:[0,0,0]
	v_mfma_scale_f32_16x16x128_f8f6f4 v[124:127], v[128:135], v[24:31], v[124:127], v183, v183 op_sel_hi:[0,0,0]
	s_mov_b32 m0, s14
	v_mfma_scale_f32_16x16x128_f8f6f4 v[108:111], v[8:15], v[40:47], v[176:179], v183, v183 op_sel_hi:[0,0,0]
	global_load_lds_dwordx4 v169, s[36:37]
	v_mfma_scale_f32_16x16x128_f8f6f4 v[104:107], v[128:135], v[40:47], v[192:195], v183, v183 op_sel_hi:[0,0,0]
	v_mfma_scale_f32_16x16x128_f8f6f4 v[92:95], v[8:15], v[56:63], v[196:199], v183, v183 op_sel_hi:[0,0,0]
	s_mov_b32 m0, s15
	v_mfma_scale_f32_16x16x128_f8f6f4 v[88:91], v[128:135], v[56:63], v[200:203], v183, v183 op_sel_hi:[0,0,0]
	global_load_lds_dwordx4 v181, s[36:37]
	v_mfma_scale_f32_16x16x128_f8f6f4 v[76:79], v[8:15], v[136:143], v[204:207], v183, v183 op_sel_hi:[0,0,0]
	s_nop 5
	v_mov_b32_e32 v200, v170
	v_mfma_scale_f32_16x16x128_f8f6f4 v[72:75], v[128:135], v[136:143], v[208:211], v183, v183 op_sel_hi:[0,0,0]
	s_setprio 0
	s_barrier
	s_add_i32 s36, 0, 0x1c000
	v_add_u32_e32 v64, s36, v200
	ds_read_b128 v[144:147], v64
	ds_read_b128 v[148:151], v64 offset:1024
	ds_read_b128 v[152:155], v64 offset:2048
	ds_read_b128 v[156:159], v64 offset:3072
	s_add_i32 s35, s35, s33
	v_mov_b32_e32 v170, v168
	v_lshl_add_u64 v[64:65], s[8:9], 0, v[170:171]
	v_lshl_add_u64 v[64:65], v[64:65], 0, s[62:63]
	s_barrier
	s_waitcnt lgkmcnt(0)
	s_setprio 1
	s_waitcnt lgkmcnt(0)
	v_mfma_scale_f32_16x16x128_f8f6f4 v[116:119], v[24:31], v[144:151], v[116:119], v183, v183 op_sel_hi:[0,0,0]
	v_mfma_scale_f32_16x16x128_f8f6f4 v[112:115], v[24:31], v[152:159], v[112:115], v183, v183 op_sel_hi:[0,0,0]
	s_add_u32 s98, s8, s62
	s_addc_u32 s99, s9, s63
	s_mov_b32 m0, s35
	v_mfma_scale_f32_16x16x128_f8f6f4 v[100:103], v[40:47], v[144:151], v[212:215], v183, v183 op_sel_hi:[0,0,0]
	global_load_lds_dwordx4 v180, s[98:99]
	v_mfma_scale_f32_16x16x128_f8f6f4 v[96:99], v[40:47], v[152:159], v[216:219], v183, v183 op_sel_hi:[0,0,0]
	s_nop 5
	v_mov_b32_e32 v212, v168
	v_mfma_scale_f32_16x16x128_f8f6f4 v[84:87], v[56:63], v[144:151], v[220:223], v183, v183 op_sel_hi:[0,0,0]
	s_add_i32 m0, s35, 0x2000
	v_mfma_scale_f32_16x16x128_f8f6f4 v[80:83], v[56:63], v[152:159], v[160:163], v183, v183 op_sel_hi:[0,0,0]
	global_load_lds_dwordx4 v168, s[98:99]
	v_mfma_scale_f32_16x16x128_f8f6f4 v[68:71], v[136:143], v[144:151], v[164:167], v183, v183 op_sel_hi:[0,0,0]
	v_mfma_scale_f32_16x16x128_f8f6f4 v[64:67], v[136:143], v[152:159], v[184:187], v183, v183 op_sel_hi:[0,0,0]
	s_setprio 0
	s_barrier
	ds_read_b128 v[136:139], v182 offset:49152
	ds_read_b128 v[140:143], v182 offset:50176
	ds_read_b128 v[160:163], v182 offset:51200
	ds_read_b128 v[164:167], v182 offset:52224
	ds_read_b128 v[184:187], v182 offset:53248
	ds_read_b128 v[188:191], v182 offset:54272
	ds_read_b128 v[192:195], v182 offset:55296
	ds_read_b128 v[196:199], v182 offset:56320
	v_mov_b32_e32 v170, v181
	v_lshl_add_u64 v[24:25], s[6:7], 0, v[170:171]
	v_lshl_add_u64 v[24:25], v[24:25], 0, s[62:63]
	s_barrier
	s_waitcnt lgkmcnt(0)
	s_setprio 1
	s_waitcnt lgkmcnt(0)
	v_mfma_scale_f32_16x16x128_f8f6f4 v[60:63], v[8:15], v[136:143], v[224:227], v183, v183 op_sel_hi:[0,0,0]
	v_mfma_scale_f32_16x16x128_f8f6f4 v[56:59], v[128:135], v[136:143], v[228:231], v183, v183 op_sel_hi:[0,0,0]
	s_add_u32 s98, s6, s62
	s_addc_u32 s99, s7, s63
	s_mov_b32 m0, s16
	v_mfma_scale_f32_16x16x128_f8f6f4 v[44:47], v[8:15], v[160:167], v[232:235], v183, v183 op_sel_hi:[0,0,0]
	global_load_lds_dwordx4 v169, s[98:99]
	v_mfma_scale_f32_16x16x128_f8f6f4 v[40:43], v[128:135], v[160:167], v[236:239], v183, v183 op_sel_hi:[0,0,0]
	v_mfma_scale_f32_16x16x128_f8f6f4 v[28:31], v[8:15], v[184:191], v[240:243], v183, v183 op_sel_hi:[0,0,0]
	s_mov_b32 m0, s17
	v_mfma_scale_f32_16x16x128_f8f6f4 v[24:27], v[128:135], v[184:191], v[244:247], v183, v183 op_sel_hi:[0,0,0]
	global_load_lds_dwordx4 v181, s[98:99]
	v_mfma_scale_f32_16x16x128_f8f6f4 v[12:15], v[8:15], v[192:199], v[248:251], v183, v183 op_sel_hi:[0,0,0]
	v_mfma_scale_f32_16x16x128_f8f6f4 v[8:11], v[128:135], v[192:199], v[172:175], v183, v183 op_sel_hi:[0,0,0]
	s_setprio 0
	s_barrier
	s_add_i32 s6, s36, s33
	s_mov_b32 s100, s6
	s_add_i32 s101, s6, 0x2000
	s_waitcnt vmcnt(4)
	s_barrier
	s_setprio 1
	v_mfma_scale_f32_16x16x128_f8f6f4 v[52:55], v[136:143], v[144:151], v[52:55], v183, v183 op_sel_hi:[0,0,0]
	v_mfma_scale_f32_16x16x128_f8f6f4 v[48:51], v[136:143], v[152:159], v[48:51], v183, v183 op_sel_hi:[0,0,0]
	s_add_u32 s98, s30, s62
	s_addc_u32 s99, s31, s63
	s_mov_b32 m0, s100
	v_mfma_scale_f32_16x16x128_f8f6f4 v[36:39], v[160:167], v[144:151], v[36:39], v183, v183 op_sel_hi:[0,0,0]
	global_load_lds_dwordx4 v180, s[98:99]
	v_mfma_scale_f32_16x16x128_f8f6f4 v[32:35], v[160:167], v[152:159], v[32:35], v183, v183 op_sel_hi:[0,0,0]
	v_mfma_scale_f32_16x16x128_f8f6f4 v[20:23], v[184:191], v[144:151], v[20:23], v183, v183 op_sel_hi:[0,0,0]
	s_mov_b32 m0, s101
	v_mfma_scale_f32_16x16x128_f8f6f4 v[16:19], v[184:191], v[152:159], v[16:19], v183, v183 op_sel_hi:[0,0,0]
	global_load_lds_dwordx4 v168, s[98:99]
	v_mfma_scale_f32_16x16x128_f8f6f4 v[4:7], v[192:199], v[144:151], v[4:7], v183, v183 op_sel_hi:[0,0,0]
	v_mfma_scale_f32_16x16x128_f8f6f4 v[0:3], v[192:199], v[152:159], v[0:3], v183, v183 op_sel_hi:[0,0,0]
	s_setprio 0
	s_add_u32 s4, s4, 0x100
	s_addc_u32 s5, s5, 0
	s_add_u32 s25, s25, 0x100
	s_addc_u32 s27, s27, 0
	s_cmp_ge_i32 s34, s13
	s_mov_b32 s6, s34
	s_barrier
	s_cbranch_scc0 .LBB0_3995

.LBB0_4066:
	s_add_i32 s34, s6, 2
	s_add_u32 s8, s4, 0xfffe0080
	s_addc_u32 s7, s5, -1
	s_add_i32 s30, 0, 0x10000
	v_add_u32_e32 v140, s30, v181
	ds_read_b128 v[128:131], v140
	ds_read_b128 v[132:135], v140 offset:1024
	ds_read_b128 v[136:139], v140 offset:2048
	ds_read_b128 v[140:143], v140 offset:3072
	s_cmp_eq_u32 s12, s6
	s_cselect_b32 s6, s52, s8
	s_cselect_b32 s7, s53, s7
	s_cselect_b32 s9, s55, s27
	s_cselect_b32 s8, s54, s25
	v_mov_b32_e32 v168, v169
	ds_read_b128 v[144:147], v182
	ds_read_b128 v[148:151], v182 offset:1024
	ds_read_b128 v[152:155], v182 offset:2048
	ds_read_b128 v[156:159], v182 offset:3072
	ds_read_b128 v[160:163], v182 offset:4096
	ds_read_b128 v[164:167], v182 offset:5120
	ds_read_b128 v[184:187], v182 offset:6144
	ds_read_b128 v[188:191], v182 offset:7168
	s_add_i32 m0, s3, 0xc000
	s_nop 0
	global_load_lds_dwordx4 v168, s[4:5]
	v_mov_b32_e32 v168, v200
	s_add_i32 m0, s3, 0xe000
	s_nop 0
	global_load_lds_dwordx4 v168, s[4:5]
	s_waitcnt lgkmcnt(8)
	s_barrier
	s_waitcnt lgkmcnt(0)
	s_setprio 1
	s_waitcnt lgkmcnt(0)
	v_mfma_scale_f32_16x16x128_f8f6f4 v[120:123], v[128:135], v[144:151], v[120:123], v183, v183 op_sel_hi:[0,0,0]
	v_mov_b32_e32 v170, v200
	v_mfma_scale_f32_16x16x128_f8f6f4 v[124:127], v[136:143], v[144:151], v[124:127], v183, v183 op_sel_hi:[0,0,0]
	v_mfma_scale_f32_16x16x128_f8f6f4 v[200:203], v[128:135], v[160:167], v[92:95], v183, v183 op_sel_hi:[0,0,0]
	v_mfma_scale_f32_16x16x128_f8f6f4 v[192:195], v[128:135], v[152:159], v[108:111], v183, v183 op_sel_hi:[0,0,0]
	v_mfma_scale_f32_16x16x128_f8f6f4 v[196:199], v[136:143], v[152:159], v[104:107], v183, v183 op_sel_hi:[0,0,0]
	v_mfma_scale_f32_16x16x128_f8f6f4 v[204:207], v[136:143], v[160:167], v[88:91], v183, v183 op_sel_hi:[0,0,0]
	v_mfma_scale_f32_16x16x128_f8f6f4 v[208:211], v[128:135], v[184:191], v[76:79], v183, v183 op_sel_hi:[0,0,0]
	v_mfma_scale_f32_16x16x128_f8f6f4 v[212:215], v[136:143], v[184:191], v[72:75], v183, v183 op_sel_hi:[0,0,0]
	s_setprio 0
	s_barrier
	s_add_i32 s35, 0, 0x14000
	v_add_u32_e32 v92, s35, v181
	v_mov_b32_e32 v104, v216
	s_add_i32 s30, s30, s33
	s_nop 0
	ds_read_b128 v[72:75], v92
	ds_read_b128 v[76:79], v92 offset:1024
	ds_read_b128 v[88:91], v92 offset:2048
	ds_read_b128 v[92:95], v92 offset:3072
	s_mov_b32 m0, s30
	s_nop 0
	global_load_lds_dwordx4 v104, s[8:9]
	v_mov_b32_e32 v104, v180
	s_add_i32 m0, s30, 0x2000
	s_nop 0
	global_load_lds_dwordx4 v104, s[8:9]
	s_barrier
	s_waitcnt lgkmcnt(0)
	s_setprio 1
	s_waitcnt lgkmcnt(0)
	v_mfma_scale_f32_16x16x128_f8f6f4 v[116:119], v[72:79], v[144:151], v[116:119], v183, v183 op_sel_hi:[0,0,0]
	v_mov_b32_e32 v168, v216
	v_mfma_scale_f32_16x16x128_f8f6f4 v[112:115], v[88:95], v[144:151], v[112:115], v183, v183 op_sel_hi:[0,0,0]
	v_mfma_scale_f32_16x16x128_f8f6f4 v[216:219], v[72:79], v[152:159], v[100:103], v183, v183 op_sel_hi:[0,0,0]
	v_mfma_scale_f32_16x16x128_f8f6f4 v[220:223], v[88:95], v[152:159], v[96:99], v183, v183 op_sel_hi:[0,0,0]
	v_mfma_scale_f32_16x16x128_f8f6f4 v[224:227], v[72:79], v[160:167], v[84:87], v183, v183 op_sel_hi:[0,0,0]
	v_mfma_scale_f32_16x16x128_f8f6f4 v[160:163], v[88:95], v[160:167], v[80:83], v183, v183 op_sel_hi:[0,0,0]
	v_mfma_scale_f32_16x16x128_f8f6f4 v[164:167], v[72:79], v[184:191], v[68:71], v183, v183 op_sel_hi:[0,0,0]
	v_mfma_scale_f32_16x16x128_f8f6f4 v[184:187], v[88:95], v[184:191], v[64:67], v183, v183 op_sel_hi:[0,0,0]
	s_setprio 0
	s_barrier
	s_nop 2
	ds_read_b128 v[64:67], v182 offset:16384
	ds_read_b128 v[68:71], v182 offset:17408
	ds_read_b128 v[80:83], v182 offset:18432
	ds_read_b128 v[84:87], v182 offset:19456
	ds_read_b128 v[96:99], v182 offset:20480
	ds_read_b128 v[100:103], v182 offset:21504
	ds_read_b128 v[104:107], v182 offset:22528
	ds_read_b128 v[108:111], v182 offset:23552
	s_nop 0
	s_nop 0
	s_barrier
	s_waitcnt lgkmcnt(0)
	s_setprio 1
	s_waitcnt lgkmcnt(0)
	v_mfma_scale_f32_16x16x128_f8f6f4 v[228:231], v[128:135], v[64:71], v[60:63], v183, v183 op_sel_hi:[0,0,0]
	v_mfma_scale_f32_16x16x128_f8f6f4 v[232:235], v[136:143], v[64:71], v[56:59], v183, v183 op_sel_hi:[0,0,0]
	s_mov_b32 m0, s3
	v_mfma_scale_f32_16x16x128_f8f6f4 v[236:239], v[128:135], v[80:87], v[44:47], v183, v183 op_sel_hi:[0,0,0]
	global_load_lds_dwordx4 v169, s[6:7]
	v_mfma_scale_f32_16x16x128_f8f6f4 v[240:243], v[136:143], v[80:87], v[40:43], v183, v183 op_sel_hi:[0,0,0]
	v_mfma_scale_f32_16x16x128_f8f6f4 v[244:247], v[128:135], v[96:103], v[28:31], v183, v183 op_sel_hi:[0,0,0]
	s_mov_b32 m0, s11
	v_mfma_scale_f32_16x16x128_f8f6f4 v[248:251], v[136:143], v[96:103], v[24:27], v183, v183 op_sel_hi:[0,0,0]
	global_load_lds_dwordx4 v170, s[6:7]
	v_mfma_scale_f32_16x16x128_f8f6f4 v[172:175], v[128:135], v[104:111], v[12:15], v183, v183 op_sel_hi:[0,0,0]
	v_mfma_scale_f32_16x16x128_f8f6f4 v[176:179], v[136:143], v[104:111], v[8:11], v183, v183 op_sel_hi:[0,0,0]
	s_setprio 0
	s_barrier
	s_add_u32 s30, s8, s20
	s_addc_u32 s31, s9, s21
	s_nop 2
	s_add_i32 s35, s35, s33
	s_mov_b32 s100, s35
	s_nop 0
	s_add_i32 s101, s35, 0x2000
	s_nop 0
	s_waitcnt vmcnt(4)
	s_barrier
	s_setprio 1
	v_mfma_scale_f32_16x16x128_f8f6f4 v[52:55], v[72:79], v[64:71], v[52:55], v183, v183 op_sel_hi:[0,0,0]
	v_mfma_scale_f32_16x16x128_f8f6f4 v[48:51], v[88:95], v[64:71], v[48:51], v183, v183 op_sel_hi:[0,0,0]
	s_mov_b32 m0, s100
	v_mfma_scale_f32_16x16x128_f8f6f4 v[36:39], v[72:79], v[80:87], v[36:39], v183, v183 op_sel_hi:[0,0,0]
	global_load_lds_dwordx4 v168, s[30:31]
	v_mfma_scale_f32_16x16x128_f8f6f4 v[32:35], v[88:95], v[80:87], v[32:35], v183, v183 op_sel_hi:[0,0,0]
	v_mfma_scale_f32_16x16x128_f8f6f4 v[20:23], v[72:79], v[96:103], v[20:23], v183, v183 op_sel_hi:[0,0,0]
	s_mov_b32 m0, s101
	v_mfma_scale_f32_16x16x128_f8f6f4 v[16:19], v[88:95], v[96:103], v[16:19], v183, v183 op_sel_hi:[0,0,0]
	global_load_lds_dwordx4 v180, s[30:31]
	v_mfma_scale_f32_16x16x128_f8f6f4 v[4:7], v[72:79], v[104:111], v[4:7], v183, v183 op_sel_hi:[0,0,0]
	v_mfma_scale_f32_16x16x128_f8f6f4 v[0:3], v[88:95], v[104:111], v[0:3], v183, v183 op_sel_hi:[0,0,0]
	s_setprio 0
	s_add_i32 s35, 0, 0x18000
	v_add_u32_e32 v24, s35, v181
	s_barrier
	ds_read_b128 v[8:11], v24
	ds_read_b128 v[12:15], v24 offset:1024
	ds_read_b128 v[128:131], v24 offset:2048
	ds_read_b128 v[132:135], v24 offset:3072
	s_add_u32 s36, s6, 0x20000
	ds_read_b128 v[24:27], v182 offset:32768
	ds_read_b128 v[28:31], v182 offset:33792
	ds_read_b128 v[40:43], v182 offset:34816
	ds_read_b128 v[44:47], v182 offset:35840
	ds_read_b128 v[56:59], v182 offset:36864
	ds_read_b128 v[60:63], v182 offset:37888
	ds_read_b128 v[136:139], v182 offset:38912
	ds_read_b128 v[140:143], v182 offset:39936
	s_addc_u32 s37, s7, 0
	s_nop 0
	s_nop 0
	s_waitcnt lgkmcnt(8)
	s_barrier
	s_waitcnt lgkmcnt(0)
	s_setprio 1
	s_waitcnt lgkmcnt(0)
	v_mfma_scale_f32_16x16x128_f8f6f4 v[120:123], v[8:15], v[24:31], v[120:123], v183, v183 op_sel_hi:[0,0,0]
	v_mfma_scale_f32_16x16x128_f8f6f4 v[124:127], v[128:135], v[24:31], v[124:127], v183, v183 op_sel_hi:[0,0,0]
	s_mov_b32 m0, s14
	v_mfma_scale_f32_16x16x128_f8f6f4 v[108:111], v[8:15], v[40:47], v[192:195], v183, v183 op_sel_hi:[0,0,0]
	global_load_lds_dwordx4 v169, s[36:37]
	v_mfma_scale_f32_16x16x128_f8f6f4 v[104:107], v[128:135], v[40:47], v[196:199], v183, v183 op_sel_hi:[0,0,0]
	v_mfma_scale_f32_16x16x128_f8f6f4 v[92:95], v[8:15], v[56:63], v[200:203], v183, v183 op_sel_hi:[0,0,0]
	s_mov_b32 m0, s15
	v_mfma_scale_f32_16x16x128_f8f6f4 v[88:91], v[128:135], v[56:63], v[204:207], v183, v183 op_sel_hi:[0,0,0]
	global_load_lds_dwordx4 v170, s[36:37]
	s_nop 5
	v_mov_b32_e32 v200, v170
	v_mfma_scale_f32_16x16x128_f8f6f4 v[76:79], v[8:15], v[136:143], v[208:211], v183, v183 op_sel_hi:[0,0,0]
	v_mfma_scale_f32_16x16x128_f8f6f4 v[72:75], v[128:135], v[136:143], v[212:215], v183, v183 op_sel_hi:[0,0,0]
	s_setprio 0
	s_barrier
	s_add_i32 s36, 0, 0x1c000
	v_add_u32_e32 v64, s36, v181
	ds_read_b128 v[144:147], v64
	ds_read_b128 v[148:151], v64 offset:1024
	ds_read_b128 v[152:155], v64 offset:2048
	ds_read_b128 v[156:159], v64 offset:3072
	s_add_i32 s35, s35, s33
	v_mov_b32_e32 v170, v180
	v_lshl_add_u64 v[64:65], s[8:9], 0, v[170:171]
	v_lshl_add_u64 v[64:65], v[64:65], 0, s[62:63]
	s_barrier
	s_waitcnt lgkmcnt(0)
	s_setprio 1
	s_waitcnt lgkmcnt(0)
	v_mfma_scale_f32_16x16x128_f8f6f4 v[116:119], v[144:151], v[24:31], v[116:119], v183, v183 op_sel_hi:[0,0,0]
	v_mfma_scale_f32_16x16x128_f8f6f4 v[112:115], v[152:159], v[24:31], v[112:115], v183, v183 op_sel_hi:[0,0,0]
	s_add_u32 s98, s8, s62
	s_addc_u32 s99, s9, s63
	s_mov_b32 m0, s35
	v_mfma_scale_f32_16x16x128_f8f6f4 v[100:103], v[144:151], v[40:47], v[216:219], v183, v183 op_sel_hi:[0,0,0]
	global_load_lds_dwordx4 v168, s[98:99]
	v_mfma_scale_f32_16x16x128_f8f6f4 v[96:99], v[152:159], v[40:47], v[220:223], v183, v183 op_sel_hi:[0,0,0]
	s_nop 5
	v_mov_b32_e32 v216, v168
	v_mfma_scale_f32_16x16x128_f8f6f4 v[84:87], v[144:151], v[56:63], v[224:227], v183, v183 op_sel_hi:[0,0,0]
	s_add_i32 m0, s35, 0x2000
	v_mfma_scale_f32_16x16x128_f8f6f4 v[80:83], v[152:159], v[56:63], v[160:163], v183, v183 op_sel_hi:[0,0,0]
	global_load_lds_dwordx4 v180, s[98:99]
	v_mfma_scale_f32_16x16x128_f8f6f4 v[68:71], v[144:151], v[136:143], v[164:167], v183, v183 op_sel_hi:[0,0,0]
	v_mfma_scale_f32_16x16x128_f8f6f4 v[64:67], v[152:159], v[136:143], v[184:187], v183, v183 op_sel_hi:[0,0,0]
	s_setprio 0
	s_barrier
	ds_read_b128 v[136:139], v182 offset:49152
	ds_read_b128 v[140:143], v182 offset:50176
	ds_read_b128 v[160:163], v182 offset:51200
	ds_read_b128 v[164:167], v182 offset:52224
	ds_read_b128 v[184:187], v182 offset:53248
	ds_read_b128 v[188:191], v182 offset:54272
	ds_read_b128 v[192:195], v182 offset:55296
	ds_read_b128 v[196:199], v182 offset:56320
	v_mov_b32_e32 v170, v200
	v_lshl_add_u64 v[24:25], s[6:7], 0, v[170:171]
	v_lshl_add_u64 v[24:25], v[24:25], 0, s[62:63]
	s_barrier
	s_waitcnt lgkmcnt(0)
	s_setprio 1
	s_waitcnt lgkmcnt(0)
	v_mfma_scale_f32_16x16x128_f8f6f4 v[60:63], v[8:15], v[136:143], v[228:231], v183, v183 op_sel_hi:[0,0,0]
	v_mfma_scale_f32_16x16x128_f8f6f4 v[56:59], v[128:135], v[136:143], v[232:235], v183, v183 op_sel_hi:[0,0,0]
	s_add_u32 s98, s6, s62
	s_addc_u32 s99, s7, s63
	s_mov_b32 m0, s16
	v_mfma_scale_f32_16x16x128_f8f6f4 v[44:47], v[8:15], v[160:167], v[236:239], v183, v183 op_sel_hi:[0,0,0]
	global_load_lds_dwordx4 v169, s[98:99]
	v_mfma_scale_f32_16x16x128_f8f6f4 v[40:43], v[128:135], v[160:167], v[240:243], v183, v183 op_sel_hi:[0,0,0]
	v_mfma_scale_f32_16x16x128_f8f6f4 v[28:31], v[8:15], v[184:191], v[244:247], v183, v183 op_sel_hi:[0,0,0]
	s_mov_b32 m0, s17
	v_mfma_scale_f32_16x16x128_f8f6f4 v[24:27], v[128:135], v[184:191], v[248:251], v183, v183 op_sel_hi:[0,0,0]
	global_load_lds_dwordx4 v200, s[98:99]
	v_mfma_scale_f32_16x16x128_f8f6f4 v[12:15], v[8:15], v[192:199], v[172:175], v183, v183 op_sel_hi:[0,0,0]
	v_mfma_scale_f32_16x16x128_f8f6f4 v[8:11], v[128:135], v[192:199], v[176:179], v183, v183 op_sel_hi:[0,0,0]
	s_setprio 0
	s_barrier
	s_add_i32 s6, s36, s33
	s_mov_b32 s100, s6
	s_add_i32 s101, s6, 0x2000
	s_waitcnt vmcnt(4)
	s_barrier
	s_setprio 1
	v_mfma_scale_f32_16x16x128_f8f6f4 v[52:55], v[144:151], v[136:143], v[52:55], v183, v183 op_sel_hi:[0,0,0]
	v_mfma_scale_f32_16x16x128_f8f6f4 v[48:51], v[152:159], v[136:143], v[48:51], v183, v183 op_sel_hi:[0,0,0]
	s_add_u32 s98, s30, s62
	s_addc_u32 s99, s31, s63
	s_mov_b32 m0, s100
	v_mfma_scale_f32_16x16x128_f8f6f4 v[36:39], v[144:151], v[160:167], v[36:39], v183, v183 op_sel_hi:[0,0,0]
	global_load_lds_dwordx4 v168, s[98:99]
	v_mfma_scale_f32_16x16x128_f8f6f4 v[32:35], v[152:159], v[160:167], v[32:35], v183, v183 op_sel_hi:[0,0,0]
	v_mfma_scale_f32_16x16x128_f8f6f4 v[20:23], v[144:151], v[184:191], v[20:23], v183, v183 op_sel_hi:[0,0,0]
	s_mov_b32 m0, s101
	v_mfma_scale_f32_16x16x128_f8f6f4 v[16:19], v[152:159], v[184:191], v[16:19], v183, v183 op_sel_hi:[0,0,0]
	global_load_lds_dwordx4 v180, s[98:99]
	v_mfma_scale_f32_16x16x128_f8f6f4 v[4:7], v[144:151], v[192:199], v[4:7], v183, v183 op_sel_hi:[0,0,0]
	v_mfma_scale_f32_16x16x128_f8f6f4 v[0:3], v[152:159], v[192:199], v[0:3], v183, v183 op_sel_hi:[0,0,0]
	s_setprio 0
	s_add_u32 s4, s4, 0x100
	s_addc_u32 s5, s5, 0
	s_add_u32 s25, s25, 0x100
	s_addc_u32 s27, s27, 0
	s_cmp_ge_i32 s34, s13
	s_mov_b32 s6, s34
	s_barrier
	s_cbranch_scc0 .LBB0_4066

.LBB0_4932:
	ds_read_b128 v[146:149], v141
	ds_read_b128 v[150:153], v141 offset:1024
	ds_read_b128 v[154:157], v141 offset:2048
	ds_read_b128 v[158:161], v141 offset:3072
	s_add_u32 s22, s20, 0xfffc0080
	s_addc_u32 s23, s21, -1
	s_cmp_eq_u32 s50, 12
	s_cselect_b32 s25, s15, s23
	s_cselect_b32 s24, s14, s22
	s_cselect_b32 s23, s17, s13
	s_cselect_b32 s22, s16, s11
	ds_read_b128 v[162:165], v142
	ds_read_b128 v[166:169], v142 offset:1024
	ds_read_b128 v[170:173], v142 offset:2048
	ds_read_b128 v[174:177], v142 offset:3072
	ds_read_b128 v[178:181], v142 offset:4096
	ds_read_b128 v[182:185], v142 offset:5120
	ds_read_b128 v[186:189], v142 offset:6144
	ds_read_b128 v[190:193], v142 offset:7168
	s_nop 0
	s_nop 0
	s_waitcnt lgkmcnt(8)
	s_barrier
	s_waitcnt lgkmcnt(0)
	s_setprio 1
	s_waitcnt lgkmcnt(0)
	v_mfma_scale_f32_16x16x128_f8f6f4 v[124:127], v[146:153], v[162:169], v[124:127], v143, v143 op_sel_hi:[0,0,0]
	v_mfma_scale_f32_16x16x128_f8f6f4 v[120:123], v[154:161], v[162:169], v[120:123], v143, v143 op_sel_hi:[0,0,0]
	s_add_i32 m0, s19, 0xc000
	v_mfma_scale_f32_16x16x128_f8f6f4 v[116:119], v[146:153], v[170:177], v[116:119], v143, v143 op_sel_hi:[0,0,0]
	global_load_lds_dwordx4 v138, s[20:21]
	v_mfma_scale_f32_16x16x128_f8f6f4 v[112:115], v[154:161], v[170:177], v[112:115], v143, v143 op_sel_hi:[0,0,0]
	v_mfma_scale_f32_16x16x128_f8f6f4 v[132:135], v[146:153], v[178:185], v[108:111], v143, v143 op_sel_hi:[0,0,0]
	s_add_i32 m0, s19, 0xe000
	v_mfma_scale_f32_16x16x128_f8f6f4 v[194:197], v[154:161], v[178:185], v[104:107], v143, v143 op_sel_hi:[0,0,0]
	global_load_lds_dwordx4 v139, s[20:21]
	v_mfma_scale_f32_16x16x128_f8f6f4 v[198:201], v[146:153], v[186:193], v[100:103], v143, v143 op_sel_hi:[0,0,0]
	v_mfma_scale_f32_16x16x128_f8f6f4 v[202:205], v[154:161], v[186:193], v[96:99], v143, v143 op_sel_hi:[0,0,0]
	s_setprio 0
	s_barrier
	s_add_i32 s51, s44, s28
	s_nop 2
	ds_read_b128 v[96:99], v144
	ds_read_b128 v[100:103], v144 offset:1024
	ds_read_b128 v[104:107], v144 offset:2048
	ds_read_b128 v[108:111], v144 offset:3072
	s_nop 0
	s_nop 0
	s_barrier
	s_waitcnt lgkmcnt(0)
	s_setprio 1
	s_waitcnt lgkmcnt(0)
	v_mfma_scale_f32_16x16x128_f8f6f4 v[206:209], v[96:103], v[162:169], v[60:63], v143, v143 op_sel_hi:[0,0,0]
	v_mfma_scale_f32_16x16x128_f8f6f4 v[162:165], v[104:111], v[162:169], v[56:59], v143, v143 op_sel_hi:[0,0,0]
	s_mov_b32 m0, s51
	v_mfma_scale_f32_16x16x128_f8f6f4 v[166:169], v[96:103], v[170:177], v[52:55], v143, v143 op_sel_hi:[0,0,0]
	global_load_lds_dwordx4 v138, s[22:23]
	v_mfma_scale_f32_16x16x128_f8f6f4 v[170:173], v[104:111], v[170:177], v[48:51], v143, v143 op_sel_hi:[0,0,0]
	v_mfma_scale_f32_16x16x128_f8f6f4 v[174:177], v[96:103], v[178:185], v[44:47], v143, v143 op_sel_hi:[0,0,0]
	s_add_i32 m0, s51, 0x2000
	v_mfma_scale_f32_16x16x128_f8f6f4 v[178:181], v[104:111], v[178:185], v[40:43], v143, v143 op_sel_hi:[0,0,0]
	global_load_lds_dwordx4 v139, s[22:23]
	v_mfma_scale_f32_16x16x128_f8f6f4 v[182:185], v[96:103], v[186:193], v[36:39], v143, v143 op_sel_hi:[0,0,0]
	v_mfma_scale_f32_16x16x128_f8f6f4 v[186:189], v[104:111], v[186:193], v[32:35], v143, v143 op_sel_hi:[0,0,0]
	s_setprio 0
	s_barrier
	s_nop 2
	ds_read_b128 v[32:35], v142 offset:16384
	ds_read_b128 v[36:39], v142 offset:17408
	ds_read_b128 v[40:43], v142 offset:18432
	ds_read_b128 v[44:47], v142 offset:19456
	ds_read_b128 v[48:51], v142 offset:20480
	ds_read_b128 v[52:55], v142 offset:21504
	ds_read_b128 v[56:59], v142 offset:22528
	ds_read_b128 v[60:63], v142 offset:23552
	s_nop 0
	s_nop 0
	s_barrier
	s_waitcnt lgkmcnt(0)
	s_setprio 1
	s_waitcnt lgkmcnt(0)
	v_mfma_scale_f32_16x16x128_f8f6f4 v[92:95], v[146:153], v[32:39], v[92:95], v143, v143 op_sel_hi:[0,0,0]
	v_mfma_scale_f32_16x16x128_f8f6f4 v[88:91], v[154:161], v[32:39], v[88:91], v143, v143 op_sel_hi:[0,0,0]
	s_mov_b32 m0, s19
	v_mfma_scale_f32_16x16x128_f8f6f4 v[84:87], v[146:153], v[40:47], v[84:87], v143, v143 op_sel_hi:[0,0,0]
	global_load_lds_dwordx4 v138, s[24:25]
	v_mfma_scale_f32_16x16x128_f8f6f4 v[80:83], v[154:161], v[40:47], v[80:83], v143, v143 op_sel_hi:[0,0,0]
	v_mfma_scale_f32_16x16x128_f8f6f4 v[76:79], v[146:153], v[48:55], v[76:79], v143, v143 op_sel_hi:[0,0,0]
	s_mov_b32 m0, s29
	v_mfma_scale_f32_16x16x128_f8f6f4 v[72:75], v[154:161], v[48:55], v[72:75], v143, v143 op_sel_hi:[0,0,0]
	global_load_lds_dwordx4 v139, s[24:25]
	v_mfma_scale_f32_16x16x128_f8f6f4 v[190:193], v[146:153], v[56:63], v[68:71], v143, v143 op_sel_hi:[0,0,0]
	v_mfma_scale_f32_16x16x128_f8f6f4 v[210:213], v[154:161], v[56:63], v[64:67], v143, v143 op_sel_hi:[0,0,0]
	s_setprio 0
	s_barrier
	s_add_u32 s52, s22, 0x40000
	s_addc_u32 s53, s23, 0
	s_nop 2
	s_add_i32 s51, s45, s28
	s_mov_b32 s100, s51
	s_nop 0
	s_add_i32 s101, s51, 0x2000
	s_nop 0
	s_waitcnt vmcnt(4)
	s_barrier
	s_setprio 1
	v_mfma_scale_f32_16x16x128_f8f6f4 v[214:217], v[96:103], v[32:39], v[28:31], v143, v143 op_sel_hi:[0,0,0]
	v_mfma_scale_f32_16x16x128_f8f6f4 v[218:221], v[104:111], v[32:39], v[24:27], v143, v143 op_sel_hi:[0,0,0]
	s_mov_b32 m0, s100
	v_mfma_scale_f32_16x16x128_f8f6f4 v[222:225], v[96:103], v[40:47], v[20:23], v143, v143 op_sel_hi:[0,0,0]
	global_load_lds_dwordx4 v138, s[52:53]
	v_mfma_scale_f32_16x16x128_f8f6f4 v[226:229], v[104:111], v[40:47], v[16:19], v143, v143 op_sel_hi:[0,0,0]
	v_mfma_scale_f32_16x16x128_f8f6f4 v[230:233], v[96:103], v[48:55], v[12:15], v143, v143 op_sel_hi:[0,0,0]
	s_mov_b32 m0, s101
	v_mfma_scale_f32_16x16x128_f8f6f4 v[234:237], v[104:111], v[48:55], v[8:11], v143, v143 op_sel_hi:[0,0,0]
	global_load_lds_dwordx4 v139, s[52:53]
	v_mfma_scale_f32_16x16x128_f8f6f4 v[238:241], v[96:103], v[56:63], v[4:7], v143, v143 op_sel_hi:[0,0,0]
	v_mfma_scale_f32_16x16x128_f8f6f4 v[242:245], v[104:111], v[56:63], v[0:3], v143, v143 op_sel_hi:[0,0,0]
	s_setprio 0
	s_add_i32 s51, 0, 0x18000
	s_nop 1
	v_add_u32_e32 v12, s51, v140
	s_barrier
	s_nop 0
	ds_read_b128 v[0:3], v12
	ds_read_b128 v[4:7], v12 offset:1024
	ds_read_b128 v[8:11], v12 offset:2048
	ds_read_b128 v[12:15], v12 offset:3072
	s_add_u32 s52, s24, 0x40000
	ds_read_b128 v[16:19], v142 offset:32768
	ds_read_b128 v[20:23], v142 offset:33792
	ds_read_b128 v[24:27], v142 offset:34816
	ds_read_b128 v[28:31], v142 offset:35840
	ds_read_b128 v[32:35], v142 offset:36864
	ds_read_b128 v[36:39], v142 offset:37888
	ds_read_b128 v[64:67], v142 offset:38912
	ds_read_b128 v[68:71], v142 offset:39936
	s_addc_u32 s53, s25, 0
	s_nop 0
	s_nop 0
	s_waitcnt lgkmcnt(8)
	s_barrier
	s_waitcnt lgkmcnt(0)
	s_setprio 1
	s_waitcnt lgkmcnt(0)
	v_mfma_scale_f32_16x16x128_f8f6f4 v[124:127], v[0:7], v[16:23], v[124:127], v143, v143 op_sel_hi:[0,0,0]
	v_mfma_scale_f32_16x16x128_f8f6f4 v[120:123], v[8:15], v[16:23], v[120:123], v143, v143 op_sel_hi:[0,0,0]
	s_mov_b32 m0, s30
	v_mfma_scale_f32_16x16x128_f8f6f4 v[116:119], v[0:7], v[24:31], v[116:119], v143, v143 op_sel_hi:[0,0,0]
	global_load_lds_dwordx4 v138, s[52:53]
	v_mfma_scale_f32_16x16x128_f8f6f4 v[112:115], v[8:15], v[24:31], v[112:115], v143, v143 op_sel_hi:[0,0,0]
	v_mfma_scale_f32_16x16x128_f8f6f4 v[108:111], v[0:7], v[32:39], v[132:135], v143, v143 op_sel_hi:[0,0,0]
	s_mov_b32 m0, s31
	v_mfma_scale_f32_16x16x128_f8f6f4 v[104:107], v[8:15], v[32:39], v[194:197], v143, v143 op_sel_hi:[0,0,0]
	global_load_lds_dwordx4 v139, s[52:53]
	v_mfma_scale_f32_16x16x128_f8f6f4 v[100:103], v[0:7], v[64:71], v[198:201], v143, v143 op_sel_hi:[0,0,0]
	v_mfma_scale_f32_16x16x128_f8f6f4 v[96:99], v[8:15], v[64:71], v[202:205], v143, v143 op_sel_hi:[0,0,0]
	s_setprio 0
	s_barrier
	s_add_i32 s52, 0, 0x1c000
	v_add_u32_e32 v40, s52, v140
	ds_read_b128 v[146:149], v40
	ds_read_b128 v[150:153], v40 offset:1024
	ds_read_b128 v[154:157], v40 offset:2048
	ds_read_b128 v[158:161], v40 offset:3072
	s_add_i32 s51, s51, s28
	v_mov_b32_e32 v128, v139
	v_lshl_add_u64 v[40:41], s[22:23], 0, v[128:129]
	v_lshl_add_u64 v[40:41], v[40:41], 0, s[6:7]
	s_barrier
	s_waitcnt lgkmcnt(0)
	s_setprio 1
	s_waitcnt lgkmcnt(0)
	v_mfma_scale_f32_16x16x128_f8f6f4 v[60:63], v[146:153], v[16:23], v[206:209], v143, v143 op_sel_hi:[0,0,0]
	v_mfma_scale_f32_16x16x128_f8f6f4 v[56:59], v[154:161], v[16:23], v[162:165], v143, v143 op_sel_hi:[0,0,0]
	s_add_u32 s98, s22, s6
	s_addc_u32 s99, s23, s7
	s_mov_b32 m0, s51
	v_mfma_scale_f32_16x16x128_f8f6f4 v[52:55], v[146:153], v[24:31], v[166:169], v143, v143 op_sel_hi:[0,0,0]
	global_load_lds_dwordx4 v138, s[98:99]
	v_mfma_scale_f32_16x16x128_f8f6f4 v[48:51], v[154:161], v[24:31], v[170:173], v143, v143 op_sel_hi:[0,0,0]
	v_mfma_scale_f32_16x16x128_f8f6f4 v[44:47], v[146:153], v[32:39], v[174:177], v143, v143 op_sel_hi:[0,0,0]
	s_add_i32 m0, s51, 0x2000
	v_mfma_scale_f32_16x16x128_f8f6f4 v[40:43], v[154:161], v[32:39], v[178:181], v143, v143 op_sel_hi:[0,0,0]
	global_load_lds_dwordx4 v139, s[98:99]
	v_mfma_scale_f32_16x16x128_f8f6f4 v[36:39], v[146:153], v[64:71], v[182:185], v143, v143 op_sel_hi:[0,0,0]
	v_mfma_scale_f32_16x16x128_f8f6f4 v[32:35], v[154:161], v[64:71], v[186:189], v143, v143 op_sel_hi:[0,0,0]
	s_setprio 0
	s_barrier
	ds_read_b128 v[16:19], v142 offset:49152
	ds_read_b128 v[20:23], v142 offset:50176
	ds_read_b128 v[162:165], v142 offset:51200
	ds_read_b128 v[166:169], v142 offset:52224
	ds_read_b128 v[170:173], v142 offset:53248
	ds_read_b128 v[174:177], v142 offset:54272
	ds_read_b128 v[178:181], v142 offset:55296
	ds_read_b128 v[182:185], v142 offset:56320
	v_mov_b32_e32 v128, v139
	v_lshl_add_u64 v[24:25], s[24:25], 0, v[128:129]
	v_lshl_add_u64 v[24:25], v[24:25], 0, s[6:7]
	s_barrier
	s_waitcnt lgkmcnt(0)
	s_setprio 1
	s_waitcnt lgkmcnt(0)
	v_mfma_scale_f32_16x16x128_f8f6f4 v[92:95], v[0:7], v[16:23], v[92:95], v143, v143 op_sel_hi:[0,0,0]
	v_mfma_scale_f32_16x16x128_f8f6f4 v[88:91], v[8:15], v[16:23], v[88:91], v143, v143 op_sel_hi:[0,0,0]
	s_add_u32 s98, s24, s6
	s_addc_u32 s99, s25, s7
	s_mov_b32 m0, s41
	v_mfma_scale_f32_16x16x128_f8f6f4 v[84:87], v[0:7], v[162:169], v[84:87], v143, v143 op_sel_hi:[0,0,0]
	global_load_lds_dwordx4 v138, s[98:99]
	v_mfma_scale_f32_16x16x128_f8f6f4 v[80:83], v[8:15], v[162:169], v[80:83], v143, v143 op_sel_hi:[0,0,0]
	v_mfma_scale_f32_16x16x128_f8f6f4 v[76:79], v[0:7], v[170:177], v[76:79], v143, v143 op_sel_hi:[0,0,0]
	s_mov_b32 m0, s42
	v_mfma_scale_f32_16x16x128_f8f6f4 v[72:75], v[8:15], v[170:177], v[72:75], v143, v143 op_sel_hi:[0,0,0]
	global_load_lds_dwordx4 v139, s[98:99]
	v_mfma_scale_f32_16x16x128_f8f6f4 v[68:71], v[0:7], v[178:185], v[190:193], v143, v143 op_sel_hi:[0,0,0]
	v_mfma_scale_f32_16x16x128_f8f6f4 v[64:67], v[8:15], v[178:185], v[210:213], v143, v143 op_sel_hi:[0,0,0]
	s_setprio 0
	s_barrier
	s_add_u32 s22, s22, 0x40080
	s_addc_u32 s23, s23, 0
	s_add_i32 s24, s52, s28
	s_nop 0
	v_mov_b32_e32 v0, v139
	s_nop 0
	s_waitcnt vmcnt(4)
	s_barrier
	s_setprio 1
	v_mfma_scale_f32_16x16x128_f8f6f4 v[28:31], v[146:153], v[16:23], v[214:217], v143, v143 op_sel_hi:[0,0,0]
	v_mfma_scale_f32_16x16x128_f8f6f4 v[24:27], v[154:161], v[16:23], v[218:221], v143, v143 op_sel_hi:[0,0,0]
	s_mov_b32 m0, s24
	v_mfma_scale_f32_16x16x128_f8f6f4 v[20:23], v[146:153], v[162:169], v[222:225], v143, v143 op_sel_hi:[0,0,0]
	global_load_lds_dwordx4 v138, s[22:23]
	v_mfma_scale_f32_16x16x128_f8f6f4 v[16:19], v[154:161], v[162:169], v[226:229], v143, v143 op_sel_hi:[0,0,0]
	v_mfma_scale_f32_16x16x128_f8f6f4 v[12:15], v[146:153], v[170:177], v[230:233], v143, v143 op_sel_hi:[0,0,0]
	s_add_i32 m0, s24, 0x2000
	v_mfma_scale_f32_16x16x128_f8f6f4 v[8:11], v[154:161], v[170:177], v[234:237], v143, v143 op_sel_hi:[0,0,0]
	global_load_lds_dwordx4 v139, s[22:23]
	v_mfma_scale_f32_16x16x128_f8f6f4 v[4:7], v[146:153], v[178:185], v[238:241], v143, v143 op_sel_hi:[0,0,0]
	v_mfma_scale_f32_16x16x128_f8f6f4 v[0:3], v[154:161], v[178:185], v[242:245], v143, v143 op_sel_hi:[0,0,0]
	s_setprio 0
	s_add_i32 s50, s50, 2
	s_add_u32 s20, s20, 0x100
	s_addc_u32 s21, s21, 0
	s_add_u32 s11, s11, 0x100
	s_addc_u32 s13, s13, 0
	s_cmp_gt_u32 s50, 13
	s_barrier
	s_cbranch_scc0 .LBB0_4932

.LBB0_5813:
	ds_read_b128 v[140:143], v134
	ds_read_b128 v[144:147], v134 offset:1024
	ds_read_b128 v[148:151], v134 offset:2048
	ds_read_b128 v[152:155], v134 offset:3072
	s_add_u32 s16, s14, 0xfffd0080
	s_addc_u32 s17, s15, -1
	s_cmp_eq_u32 s53, 8
	s_cselect_b32 s19, s13, s17
	s_cselect_b32 s18, s12, s16
	s_cselect_b32 s17, s11, s52
	s_cselect_b32 s16, s10, s51
	ds_read_b128 v[156:159], v135
	ds_read_b128 v[160:163], v135 offset:1024
	ds_read_b128 v[164:167], v135 offset:2048
	ds_read_b128 v[168:171], v135 offset:3072
	ds_read_b128 v[172:175], v135 offset:4096
	ds_read_b128 v[176:179], v135 offset:5120
	ds_read_b128 v[180:183], v135 offset:6144
	ds_read_b128 v[184:187], v135 offset:7168
	s_nop 0
	s_nop 0
	s_waitcnt lgkmcnt(8)
	s_barrier
	s_waitcnt lgkmcnt(0)
	s_setprio 1
	s_waitcnt lgkmcnt(0)
	v_mfma_scale_f32_16x16x128_f8f6f4 v[124:127], v[140:147], v[156:163], v[124:127], v136, v136 op_sel_hi:[0,0,0]
	v_mfma_scale_f32_16x16x128_f8f6f4 v[120:123], v[148:155], v[156:163], v[120:123], v136, v136 op_sel_hi:[0,0,0]
	s_mov_b32 m0, s38
	v_mfma_scale_f32_16x16x128_f8f6f4 v[116:119], v[140:147], v[164:171], v[116:119], v136, v136 op_sel_hi:[0,0,0]
	global_load_lds_dwordx4 v132, s[14:15]
	v_mfma_scale_f32_16x16x128_f8f6f4 v[112:115], v[148:155], v[164:171], v[112:115], v136, v136 op_sel_hi:[0,0,0]
	v_mfma_scale_f32_16x16x128_f8f6f4 v[188:191], v[140:147], v[172:179], v[108:111], v136, v136 op_sel_hi:[0,0,0]
	s_mov_b32 m0, s39
	v_mfma_scale_f32_16x16x128_f8f6f4 v[192:195], v[148:155], v[172:179], v[104:107], v136, v136 op_sel_hi:[0,0,0]
	global_load_lds_dwordx4 v133, s[14:15]
	v_mfma_scale_f32_16x16x128_f8f6f4 v[196:199], v[140:147], v[180:187], v[100:103], v136, v136 op_sel_hi:[0,0,0]
	v_mfma_scale_f32_16x16x128_f8f6f4 v[200:203], v[148:155], v[180:187], v[96:99], v136, v136 op_sel_hi:[0,0,0]
	s_setprio 0
	s_barrier
	s_nop 2
	ds_read_b128 v[96:99], v137
	ds_read_b128 v[100:103], v137 offset:1024
	ds_read_b128 v[104:107], v137 offset:2048
	ds_read_b128 v[108:111], v137 offset:3072
	s_nop 0
	s_nop 0
	s_barrier
	s_waitcnt lgkmcnt(0)
	s_setprio 1
	s_waitcnt lgkmcnt(0)
	v_mfma_scale_f32_16x16x128_f8f6f4 v[204:207], v[96:103], v[156:163], v[92:95], v136, v136 op_sel_hi:[0,0,0]
	v_mfma_scale_f32_16x16x128_f8f6f4 v[156:159], v[104:111], v[156:163], v[88:91], v136, v136 op_sel_hi:[0,0,0]
	s_mov_b32 m0, s40
	v_mfma_scale_f32_16x16x128_f8f6f4 v[160:163], v[96:103], v[164:171], v[84:87], v136, v136 op_sel_hi:[0,0,0]
	global_load_lds_dwordx4 v132, s[16:17]
	v_mfma_scale_f32_16x16x128_f8f6f4 v[164:167], v[104:111], v[164:171], v[80:83], v136, v136 op_sel_hi:[0,0,0]
	v_mfma_scale_f32_16x16x128_f8f6f4 v[168:171], v[96:103], v[172:179], v[76:79], v136, v136 op_sel_hi:[0,0,0]
	s_mov_b32 m0, s41
	v_mfma_scale_f32_16x16x128_f8f6f4 v[172:175], v[104:111], v[172:179], v[72:75], v136, v136 op_sel_hi:[0,0,0]
	global_load_lds_dwordx4 v133, s[16:17]
	v_mfma_scale_f32_16x16x128_f8f6f4 v[176:179], v[96:103], v[180:187], v[68:71], v136, v136 op_sel_hi:[0,0,0]
	v_mfma_scale_f32_16x16x128_f8f6f4 v[180:183], v[104:111], v[180:187], v[64:67], v136, v136 op_sel_hi:[0,0,0]
	s_setprio 0
	s_barrier
	s_nop 2
	ds_read_b128 v[64:67], v135 offset:16384
	ds_read_b128 v[68:71], v135 offset:17408
	ds_read_b128 v[72:75], v135 offset:18432
	ds_read_b128 v[76:79], v135 offset:19456
	ds_read_b128 v[80:83], v135 offset:20480
	ds_read_b128 v[84:87], v135 offset:21504
	ds_read_b128 v[88:91], v135 offset:22528
	ds_read_b128 v[92:95], v135 offset:23552
	s_nop 0
	s_nop 0
	s_barrier
	s_waitcnt lgkmcnt(0)
	s_setprio 1
	s_waitcnt lgkmcnt(0)
	v_mfma_scale_f32_16x16x128_f8f6f4 v[60:63], v[140:147], v[64:71], v[60:63], v136, v136 op_sel_hi:[0,0,0]
	v_mfma_scale_f32_16x16x128_f8f6f4 v[56:59], v[148:155], v[64:71], v[56:59], v136, v136 op_sel_hi:[0,0,0]
	s_mov_b32 m0, s24
	v_mfma_scale_f32_16x16x128_f8f6f4 v[52:55], v[140:147], v[72:79], v[52:55], v136, v136 op_sel_hi:[0,0,0]
	global_load_lds_dwordx4 v132, s[18:19]
	v_mfma_scale_f32_16x16x128_f8f6f4 v[48:51], v[148:155], v[72:79], v[48:51], v136, v136 op_sel_hi:[0,0,0]
	v_mfma_scale_f32_16x16x128_f8f6f4 v[184:187], v[140:147], v[80:87], v[44:47], v136, v136 op_sel_hi:[0,0,0]
	s_mov_b32 m0, s25
	v_mfma_scale_f32_16x16x128_f8f6f4 v[208:211], v[148:155], v[80:87], v[40:43], v136, v136 op_sel_hi:[0,0,0]
	global_load_lds_dwordx4 v133, s[18:19]
	v_mfma_scale_f32_16x16x128_f8f6f4 v[212:215], v[140:147], v[88:95], v[36:39], v136, v136 op_sel_hi:[0,0,0]
	v_mfma_scale_f32_16x16x128_f8f6f4 v[216:219], v[148:155], v[88:95], v[32:35], v136, v136 op_sel_hi:[0,0,0]
	s_setprio 0
	s_barrier
	s_add_u32 s54, s16, 0x30000
	s_nop 3
	s_addc_u32 s55, s17, 0
	s_nop 0
	s_nop 0
	s_waitcnt vmcnt(4)
	s_barrier
	s_setprio 1
	v_mfma_scale_f32_16x16x128_f8f6f4 v[220:223], v[96:103], v[64:71], v[28:31], v136, v136 op_sel_hi:[0,0,0]
	v_mfma_scale_f32_16x16x128_f8f6f4 v[224:227], v[104:111], v[64:71], v[24:27], v136, v136 op_sel_hi:[0,0,0]
	s_mov_b32 m0, s42
	v_mfma_scale_f32_16x16x128_f8f6f4 v[228:231], v[96:103], v[72:79], v[20:23], v136, v136 op_sel_hi:[0,0,0]
	global_load_lds_dwordx4 v132, s[54:55]
	v_mfma_scale_f32_16x16x128_f8f6f4 v[232:235], v[104:111], v[72:79], v[16:19], v136, v136 op_sel_hi:[0,0,0]
	v_mfma_scale_f32_16x16x128_f8f6f4 v[236:239], v[96:103], v[80:87], v[12:15], v136, v136 op_sel_hi:[0,0,0]
	s_mov_b32 m0, s43
	v_mfma_scale_f32_16x16x128_f8f6f4 v[240:243], v[104:111], v[80:87], v[8:11], v136, v136 op_sel_hi:[0,0,0]
	global_load_lds_dwordx4 v133, s[54:55]
	v_mfma_scale_f32_16x16x128_f8f6f4 v[244:247], v[96:103], v[88:95], v[4:7], v136, v136 op_sel_hi:[0,0,0]
	v_mfma_scale_f32_16x16x128_f8f6f4 v[248:251], v[104:111], v[88:95], v[0:3], v136, v136 op_sel_hi:[0,0,0]
	s_setprio 0
	s_barrier
	s_nop 4
	ds_read_b128 v[0:3], v138
	ds_read_b128 v[4:7], v138 offset:1024
	ds_read_b128 v[8:11], v138 offset:2048
	ds_read_b128 v[12:15], v138 offset:3072
	s_add_u32 s54, s18, 0x30000
	ds_read_b128 v[16:19], v135 offset:32768
	ds_read_b128 v[20:23], v135 offset:33792
	ds_read_b128 v[24:27], v135 offset:34816
	ds_read_b128 v[28:31], v135 offset:35840
	ds_read_b128 v[32:35], v135 offset:36864
	ds_read_b128 v[36:39], v135 offset:37888
	ds_read_b128 v[40:43], v135 offset:38912
	ds_read_b128 v[44:47], v135 offset:39936
	s_addc_u32 s55, s19, 0
	s_nop 0
	s_nop 0
	s_waitcnt lgkmcnt(8)
	s_barrier
	s_waitcnt lgkmcnt(0)
	s_setprio 1
	s_waitcnt lgkmcnt(0)
	v_mfma_scale_f32_16x16x128_f8f6f4 v[124:127], v[0:7], v[16:23], v[124:127], v136, v136 op_sel_hi:[0,0,0]
	v_mfma_scale_f32_16x16x128_f8f6f4 v[120:123], v[8:15], v[16:23], v[120:123], v136, v136 op_sel_hi:[0,0,0]
	s_mov_b32 m0, s26
	v_mfma_scale_f32_16x16x128_f8f6f4 v[116:119], v[0:7], v[24:31], v[116:119], v136, v136 op_sel_hi:[0,0,0]
	global_load_lds_dwordx4 v132, s[54:55]
	v_mfma_scale_f32_16x16x128_f8f6f4 v[112:115], v[8:15], v[24:31], v[112:115], v136, v136 op_sel_hi:[0,0,0]
	v_mfma_scale_f32_16x16x128_f8f6f4 v[108:111], v[0:7], v[32:39], v[188:191], v136, v136 op_sel_hi:[0,0,0]
	s_mov_b32 m0, s27
	v_mfma_scale_f32_16x16x128_f8f6f4 v[104:107], v[8:15], v[32:39], v[192:195], v136, v136 op_sel_hi:[0,0,0]
	global_load_lds_dwordx4 v133, s[54:55]
	v_mfma_scale_f32_16x16x128_f8f6f4 v[100:103], v[0:7], v[40:47], v[196:199], v136, v136 op_sel_hi:[0,0,0]
	v_mfma_scale_f32_16x16x128_f8f6f4 v[96:99], v[8:15], v[40:47], v[200:203], v136, v136 op_sel_hi:[0,0,0]
	s_setprio 0
	s_barrier
	ds_read_b128 v[140:143], v139
	ds_read_b128 v[144:147], v139 offset:1024
	ds_read_b128 v[148:151], v139 offset:2048
	ds_read_b128 v[152:155], v139 offset:3072
	v_mov_b32_e32 v128, v133
	v_lshl_add_u64 v[64:65], s[16:17], 0, v[128:129]
	v_lshl_add_u64 v[64:65], v[64:65], 0, s[4:5]
	s_barrier
	s_waitcnt lgkmcnt(0)
	s_setprio 1
	s_waitcnt lgkmcnt(0)
	v_mfma_scale_f32_16x16x128_f8f6f4 v[92:95], v[140:147], v[16:23], v[204:207], v136, v136 op_sel_hi:[0,0,0]
	v_mfma_scale_f32_16x16x128_f8f6f4 v[88:91], v[148:155], v[16:23], v[156:159], v136, v136 op_sel_hi:[0,0,0]
	s_add_u32 s98, s16, s4
	s_addc_u32 s99, s17, s5
	s_mov_b32 m0, s45
	v_mfma_scale_f32_16x16x128_f8f6f4 v[84:87], v[140:147], v[24:31], v[160:163], v136, v136 op_sel_hi:[0,0,0]
	global_load_lds_dwordx4 v132, s[98:99]
	v_mfma_scale_f32_16x16x128_f8f6f4 v[80:83], v[148:155], v[24:31], v[164:167], v136, v136 op_sel_hi:[0,0,0]
	v_mfma_scale_f32_16x16x128_f8f6f4 v[76:79], v[140:147], v[32:39], v[168:171], v136, v136 op_sel_hi:[0,0,0]
	s_mov_b32 m0, s46
	v_mfma_scale_f32_16x16x128_f8f6f4 v[72:75], v[148:155], v[32:39], v[172:175], v136, v136 op_sel_hi:[0,0,0]
	global_load_lds_dwordx4 v133, s[98:99]
	v_mfma_scale_f32_16x16x128_f8f6f4 v[68:71], v[140:147], v[40:47], v[176:179], v136, v136 op_sel_hi:[0,0,0]
	v_mfma_scale_f32_16x16x128_f8f6f4 v[64:67], v[148:155], v[40:47], v[180:183], v136, v136 op_sel_hi:[0,0,0]
	s_setprio 0
	s_barrier
	ds_read_b128 v[16:19], v135 offset:49152
	ds_read_b128 v[20:23], v135 offset:50176
	ds_read_b128 v[156:159], v135 offset:51200
	ds_read_b128 v[160:163], v135 offset:52224
	ds_read_b128 v[164:167], v135 offset:53248
	ds_read_b128 v[168:171], v135 offset:54272
	ds_read_b128 v[172:175], v135 offset:55296
	ds_read_b128 v[176:179], v135 offset:56320
	v_mov_b32_e32 v128, v133
	v_lshl_add_u64 v[24:25], s[18:19], 0, v[128:129]
	v_lshl_add_u64 v[24:25], v[24:25], 0, s[4:5]
	s_barrier
	s_waitcnt lgkmcnt(0)
	s_setprio 1
	s_waitcnt lgkmcnt(0)
	v_mfma_scale_f32_16x16x128_f8f6f4 v[60:63], v[0:7], v[16:23], v[60:63], v136, v136 op_sel_hi:[0,0,0]
	v_mfma_scale_f32_16x16x128_f8f6f4 v[56:59], v[8:15], v[16:23], v[56:59], v136, v136 op_sel_hi:[0,0,0]
	s_add_u32 s98, s18, s4
	s_addc_u32 s99, s19, s5
	s_mov_b32 m0, s35
	v_mfma_scale_f32_16x16x128_f8f6f4 v[52:55], v[0:7], v[156:163], v[52:55], v136, v136 op_sel_hi:[0,0,0]
	global_load_lds_dwordx4 v132, s[98:99]
	v_mfma_scale_f32_16x16x128_f8f6f4 v[48:51], v[8:15], v[156:163], v[48:51], v136, v136 op_sel_hi:[0,0,0]
	v_mfma_scale_f32_16x16x128_f8f6f4 v[44:47], v[0:7], v[164:171], v[184:187], v136, v136 op_sel_hi:[0,0,0]
	s_mov_b32 m0, s36
	v_mfma_scale_f32_16x16x128_f8f6f4 v[40:43], v[8:15], v[164:171], v[208:211], v136, v136 op_sel_hi:[0,0,0]
	global_load_lds_dwordx4 v133, s[98:99]
	v_mfma_scale_f32_16x16x128_f8f6f4 v[36:39], v[0:7], v[172:179], v[212:215], v136, v136 op_sel_hi:[0,0,0]
	v_mfma_scale_f32_16x16x128_f8f6f4 v[32:35], v[8:15], v[172:179], v[216:219], v136, v136 op_sel_hi:[0,0,0]
	s_setprio 0
	s_barrier
	s_add_u32 s16, s16, 0x30080
	s_addc_u32 s17, s17, 0
	s_add_i32 s18, s44, s23
	s_nop 0
	v_mov_b32_e32 v0, v133
	s_nop 0
	s_waitcnt vmcnt(4)
	s_barrier
	s_setprio 1
	v_mfma_scale_f32_16x16x128_f8f6f4 v[28:31], v[140:147], v[16:23], v[220:223], v136, v136 op_sel_hi:[0,0,0]
	v_mfma_scale_f32_16x16x128_f8f6f4 v[24:27], v[148:155], v[16:23], v[224:227], v136, v136 op_sel_hi:[0,0,0]
	s_mov_b32 m0, s18
	v_mfma_scale_f32_16x16x128_f8f6f4 v[20:23], v[140:147], v[156:163], v[228:231], v136, v136 op_sel_hi:[0,0,0]
	global_load_lds_dwordx4 v132, s[16:17]
	v_mfma_scale_f32_16x16x128_f8f6f4 v[16:19], v[148:155], v[156:163], v[232:235], v136, v136 op_sel_hi:[0,0,0]
	v_mfma_scale_f32_16x16x128_f8f6f4 v[12:15], v[140:147], v[164:171], v[236:239], v136, v136 op_sel_hi:[0,0,0]
	s_add_i32 m0, s18, 0x2000
	v_mfma_scale_f32_16x16x128_f8f6f4 v[8:11], v[148:155], v[164:171], v[240:243], v136, v136 op_sel_hi:[0,0,0]
	global_load_lds_dwordx4 v133, s[16:17]
	v_mfma_scale_f32_16x16x128_f8f6f4 v[4:7], v[140:147], v[172:179], v[244:247], v136, v136 op_sel_hi:[0,0,0]
	v_mfma_scale_f32_16x16x128_f8f6f4 v[0:3], v[148:155], v[172:179], v[248:251], v136, v136 op_sel_hi:[0,0,0]
	s_setprio 0
	s_add_i32 s53, s53, 2
	s_add_u32 s14, s14, 0x100
	s_addc_u32 s15, s15, 0
	s_add_u32 s51, s51, 0x100
	s_addc_u32 s52, s52, 0
	s_cmp_gt_u32 s53, 9
	s_barrier
	s_cbranch_scc0 .LBB0_5813
